# attention block-units remapped so that the query blocks sharing one (batch, head) K/V run on one XCD (L2 reuse); plus earlier: peeled first K-trip with C=0 (no accumulator clearing), MoE next() ballot
# speedup vs baseline: 1.0452x; 1.0218x over previous
; #define PG8_LDA(dst, b, h) do { _Pragma("unroll") for (int m = 0; m < 4; ++m) PG8_LD2(dst[m], PG8_SA(b, h) + aoff + m * 2048); } while (0)
; #define PG8_BAR __builtin_amdgcn_s_barrier()
; template <int DT  , class Epi, class Sched, class Hook = NoHook>
; __device__ __forceinline__ void gemm_phase(LAS unsigned char* lds, const Sched& S, const Epi& E, int wave_s, LAS unsigned char* aux  ,
;                                            const Hook& H = Hook()  ) {
;     ...
;         for (int t = 0; t < nt; t += 2) {
;             const bool last = (t == nt - 2);
;             const char* a1 = cA + (size_t)(t + 1) * kstep;
;             const char* a2 = last ? nA : cA + (size_t)(t + 2) * kstep; const char* b2 = last ? nB : cB + (size_t)(t + 2) * kstep;
;             const char* a3 = a2 + kstep; const char* b3 = b2 + kstep;
;             PG8_LDB(B0, 0, 0); PG8_LDB(B1, 0, 1); PG8_SCHED; PG8_LDA(At, 0, 0); PG8_STAGE_A(PG8_SA(1, 1), 1, a1);
;             if (GATHER) { if (last && has_next) S.gather_lds(nxt, gA, tid, aux + ((ui + 1) & 1) * 1024); }
;             PG8_WAIT_V(8); PG8_WAIT_L(0); PG8_BAR; PG8_MMA(0, 0, At, B0); PG8_MMA(0, 1, At, B1); PG8_BAR; PG8_SCHED;
;             PG8_LDA(At, 0, 1); PG8_STAGE(PG8_SB(0, 0), b2, voffB); PG8_STAGE(PG8_SB(0, 1), b2 + hstep, voffB); PG8_STAGE_A(PG8_SA(0, 0), 0, a2);
;             PG8_WAIT_V(8); PG8_WAIT_L(0); PG8_BAR; PG8_MMA(1, 0, At, B0); PG8_MMA(1, 1, At, B1); PG8_BAR; PG8_SCHED;
;             PG8_LDB(B0, 1, 0); PG8_LDB(B1, 1, 1); PG8_SCHED; PG8_LDA(At, 1, 0); PG8_STAGE_A(PG8_SA(0, 1), 1, a2);
;             PG8_WAIT_V(8); PG8_WAIT_L(0); PG8_BAR; PG8_MMA(0, 0, At, B0); PG8_MMA(0, 1, At, B1); PG8_BAR; PG8_SCHED;
;             PG8_LDA(At, 1, 1); PG8_STAGE(PG8_SB(1, 0), b3, voffB); PG8_STAGE(PG8_SB(1, 1), b3 + hstep, voffB); PG8_STAGE_A(PG8_SA(1, 0), 0, a3);
;             PG8_WAIT_V(8); PG8_WAIT_L(0); PG8_BAR; PG8_MMA(1, 0, At, B0); PG8_MMA(1, 1, At, B1); PG8_BAR; PG8_SCHED;
;         }
;         if (wr == 0) PG8_BAR;
;         E(acc, cur, wr, wc, fr, fq, aux + 2048 + (ui & 1) * 3072);
;         H(ui);
;         if (!has_next) break;
; #pragma unroll
;         for (int a = 0; a < 2; ++a)
; #pragma unroll
;             for (int b = 0; b < 2; ++b)
; #pragma unroll
;                 for (int m = 0; m < 4; ++m)
; #pragma unroll
;                     for (int n = 0; n < 2; ++n) acc[a][b][m][n] = (acc_t){0, 0, 0, 0};
.LBB0_118:
	s_ashr_i32 s29, s28, 31
	s_lshl_b64 s[30:31], s[28:29], 18
	s_add_u32 s30, s36, s30
	s_addc_u32 s31, s37, s31
	s_and_b64 s[34:35], s[2:3], exec
	s_cselect_b32 s29, s31, s47
	s_cselect_b32 s41, s30, s46
	s_ashr_i32 s27, s26, 31
	s_lshl_b64 s[34:35], s[26:27], 18
	s_add_u32 s34, s67, s34
	s_addc_u32 s35, s20, s35
	s_and_b64 s[72:73], s[2:3], exec
	s_cselect_b32 s27, s35, s19
	s_cselect_b32 s68, s34, s18
	s_add_u32 s46, s46, 0x20080
	s_addc_u32 s47, s47, 0
	s_add_u32 s76, s18, 0x100
	s_addc_u32 s77, s19, 0
	s_mov_b32 vcc_lo, -2
	ds_read_b128 v[130:133], v168
	ds_read_b128 v[134:137], v169
	ds_read_b128 v[138:141], v164
	ds_read_b128 v[142:145], v165
	ds_read_b128 v[158:161], v170
	ds_read_b128 v[182:185], v171
	ds_read_b128 v[186:189], v172
	ds_read_b128 v[190:193], v173
	s_add_u32 s18, s46, 0xfffe0080
	s_addc_u32 s19, s47, -1
	s_cmp_eq_u32 vcc_lo, 4
	s_cselect_b32 s73, s29, s19
	s_cselect_b32 s72, s41, s18
	s_cselect_b32 s19, s27, s77
	s_cselect_b32 s18, s68, s76
	v_lshl_add_u64 v[162:163], s[46:47], 0, v[154:155]
	s_add_i32 m0, s11, 0xc000
	ds_read_b128 v[196:199], v181
	ds_read_b128 v[204:207], v181 offset:1024
	ds_read_b128 v[208:211], v181 offset:2048
	ds_read_b128 v[212:215], v181 offset:3072
	ds_read_b128 v[216:219], v181 offset:4096
	ds_read_b128 v[226:229], v181 offset:5120
	ds_read_b128 v[230:233], v181 offset:6144
	ds_read_b128 v[234:237], v181 offset:7168
	global_load_lds_dwordx4 v[162:163], off
	v_lshl_add_u64 v[162:163], s[46:47], 0, v[156:157]
	s_add_i32 m0, s11, 0xe000
	s_nop 0
	global_load_lds_dwordx4 v[162:163], off
	s_waitcnt vmcnt(8)
	s_waitcnt lgkmcnt(0)
	s_barrier
	s_setprio 1
	s_waitcnt lgkmcnt(0)
	v_mfma_i32_16x16x64_i8 v[126:129], v[138:141], v[196:199], 0
	v_mfma_i32_16x16x64_i8 v[122:125], v[134:137], v[196:199], 0
	v_mfma_i32_16x16x64_i8 v[110:113], v[138:141], v[208:211], 0
	v_mfma_i32_16x16x64_i8 v[106:109], v[134:137], v[208:211], 0
	v_mfma_i32_16x16x64_i8 v[94:97], v[138:141], v[216:219], 0
	v_mfma_i32_16x16x64_i8 v[90:93], v[134:137], v[216:219], 0
	v_mfma_i32_16x16x64_i8 v[78:81], v[138:141], v[230:233], 0
	v_mfma_i32_16x16x64_i8 v[74:77], v[134:137], v[230:233], 0
	v_mfma_i32_16x16x64_i8 v[126:129], v[130:133], v[204:207], v[126:129]
	v_mfma_i32_16x16x64_i8 v[122:125], v[158:161], v[204:207], v[122:125]
	v_mfma_i32_16x16x64_i8 v[110:113], v[130:133], v[212:215], v[110:113]
	v_mfma_i32_16x16x64_i8 v[106:109], v[158:161], v[212:215], v[106:109]
	v_mfma_i32_16x16x64_i8 v[94:97], v[130:133], v[226:229], v[94:97]
	v_mfma_i32_16x16x64_i8 v[90:93], v[158:161], v[226:229], v[90:93]
	v_mfma_i32_16x16x64_i8 v[78:81], v[130:133], v[234:237], v[78:81]
	v_mfma_i32_16x16x64_i8 v[74:77], v[158:161], v[234:237], v[74:77]
	s_setprio 0
	s_setprio 1
	v_mfma_i32_16x16x64_i8 v[118:121], v[142:145], v[196:199], 0
	v_mfma_i32_16x16x64_i8 v[114:117], v[186:189], v[196:199], 0
	v_mfma_i32_16x16x64_i8 v[102:105], v[142:145], v[208:211], 0
	v_mfma_i32_16x16x64_i8 v[98:101], v[186:189], v[208:211], 0
	v_mfma_i32_16x16x64_i8 v[86:89], v[142:145], v[216:219], 0
	v_mfma_i32_16x16x64_i8 v[82:85], v[186:189], v[216:219], 0
	v_mfma_i32_16x16x64_i8 v[70:73], v[142:145], v[230:233], 0
	v_mfma_i32_16x16x64_i8 v[66:69], v[186:189], v[230:233], 0
	v_mfma_i32_16x16x64_i8 v[118:121], v[182:185], v[204:207], v[118:121]
	v_mfma_i32_16x16x64_i8 v[114:117], v[190:193], v[204:207], v[114:117]
	v_mfma_i32_16x16x64_i8 v[102:105], v[182:185], v[212:215], v[102:105]
	v_mfma_i32_16x16x64_i8 v[98:101], v[190:193], v[212:215], v[98:101]
	v_mfma_i32_16x16x64_i8 v[86:89], v[182:185], v[226:229], v[86:89]
	v_mfma_i32_16x16x64_i8 v[82:85], v[190:193], v[226:229], v[82:85]
	v_mfma_i32_16x16x64_i8 v[70:73], v[182:185], v[234:237], v[70:73]
	v_mfma_i32_16x16x64_i8 v[66:69], v[190:193], v[234:237], v[66:69]
	s_setprio 0
	s_barrier
	s_mov_b32 m0, s12
	v_lshl_add_u64 v[162:163], s[18:19], 0, v[150:151]
	s_add_u32 s42, s18, 0x20000
	ds_read_b128 v[196:199], v181 offset:16384
	ds_read_b128 v[204:207], v181 offset:17408
	ds_read_b128 v[208:211], v181 offset:18432
	ds_read_b128 v[212:215], v181 offset:19456
	ds_read_b128 v[216:219], v181 offset:20480
	ds_read_b128 v[226:229], v181 offset:21504
	ds_read_b128 v[230:233], v181 offset:22528
	ds_read_b128 v[234:237], v181 offset:23552
	global_load_lds_dwordx4 v[162:163], off
	v_lshl_add_u64 v[200:201], s[18:19], 0, v[146:147]
	s_mov_b32 m0, s13
	s_addc_u32 s43, s19, 0
	global_load_lds_dwordx4 v[200:201], off
	v_lshl_add_u64 v[238:239], s[42:43], 0, v[150:151]
	s_mov_b32 m0, s38
	v_lshl_add_u64 v[240:241], s[72:73], 0, v[148:149]
	global_load_lds_dwordx4 v[238:239], off
	v_lshl_add_u64 v[238:239], s[42:43], 0, v[146:147]
	s_mov_b32 m0, s51
	s_nop 0
	global_load_lds_dwordx4 v[238:239], off
	v_lshl_add_u64 v[238:239], s[72:73], 0, v[152:153]
	s_mov_b32 m0, s11
	s_nop 0
	global_load_lds_dwordx4 v[238:239], off
	s_mov_b32 m0, s89
	s_nop 0
	global_load_lds_dwordx4 v[240:241], off
	s_waitcnt vmcnt(8)
	s_waitcnt lgkmcnt(0)
	s_barrier
; #define PG8_STAGE_A(bufoff, h, abase) do { _Pragma("unroll") for (int _i = 0; _i < 2; ++_i) { \
;         const char* _src = GATHER ? ((const char*)(abase) + gA[h][_i]) : ((const char*)(abase) + (size_t)(h) * hstep + voffA[_i]); \
;         __builtin_amdgcn_global_load_lds((const unsigned*)_src, (LAS unsigned*)(lds + (bufoff) + ldsw + _i * 8192), 16, 0, 0); } } while (0)
; #define PG8_LDA(dst, b, h) do { _Pragma("unroll") for (int m = 0; m < 4; ++m) PG8_LD2(dst[m], PG8_SA(b, h) + aoff + m * 2048); } while (0)
; #define PG8_LDB(dst, b, h) do { _Pragma("unroll") for (int n = 0; n < 2; ++n) PG8_LD2(dst[n], PG8_SB(b, h) + boff + n * 2048); } while (0)
; #define PG8_WAIT_V(n) asm volatile("s_waitcnt vmcnt(" #n ")" ::: "memory")
; #define PG8_WAIT_L(n) asm volatile("s_waitcnt lgkmcnt(" #n ")" ::: "memory")
; #define PG8_BAR __builtin_amdgcn_s_barrier()
; #define PG8_SCHED __builtin_amdgcn_sched_barrier(0)
; template <int DT  , class Epi, class Sched, class Hook = NoHook>
; __device__ __forceinline__ void gemm_phase(LAS unsigned char* lds, const Sched& S, const Epi& E, int wave_s, LAS unsigned char* aux  ,
;                                            const Hook& H = Hook()  ) {
;     ...
;             PG8_WAIT_V(8); PG8_WAIT_L(0); PG8_BAR; PG8_MMA(1, 0, At, B0); PG8_MMA(1, 1, At, B1); PG8_BAR; PG8_SCHED;
;             PG8_LDB(B0, 1, 0); PG8_LDB(B1, 1, 1); PG8_SCHED; PG8_LDA(At, 1, 0); PG8_STAGE_A(PG8_SA(0, 1), 1, a2);
;             PG8_WAIT_V(8); PG8_WAIT_L(0); PG8_BAR; PG8_MMA(0, 0, At, B0); PG8_MMA(0, 1, At, B1); PG8_BAR; PG8_SCHED;
	s_setprio 1
	s_waitcnt lgkmcnt(0)
	v_mfma_i32_16x16x64_i8 v[54:57], v[138:141], v[196:199], 0
	v_mfma_i32_16x16x64_i8 v[50:53], v[134:137], v[196:199], 0
	v_mfma_i32_16x16x64_i8 v[38:41], v[138:141], v[208:211], 0
	v_mfma_i32_16x16x64_i8 v[34:37], v[134:137], v[208:211], 0
	v_mfma_i32_16x16x64_i8 v[20:23], v[138:141], v[216:219], 0
	v_mfma_i32_16x16x64_i8 v[16:19], v[134:137], v[216:219], 0
	v_mfma_i32_16x16x64_i8 v[4:7], v[138:141], v[230:233], 0
	v_mfma_i32_16x16x64_i8 v[0:3], v[134:137], v[230:233], 0
	v_mfma_i32_16x16x64_i8 v[54:57], v[130:133], v[204:207], v[54:57]
	v_mfma_i32_16x16x64_i8 v[50:53], v[158:161], v[204:207], v[50:53]
	v_mfma_i32_16x16x64_i8 v[38:41], v[130:133], v[212:215], v[38:41]
	v_mfma_i32_16x16x64_i8 v[34:37], v[158:161], v[212:215], v[34:37]
	v_mfma_i32_16x16x64_i8 v[20:23], v[130:133], v[226:229], v[20:23]
	v_mfma_i32_16x16x64_i8 v[16:19], v[158:161], v[226:229], v[16:19]
	v_mfma_i32_16x16x64_i8 v[4:7], v[130:133], v[234:237], v[4:7]
	v_mfma_i32_16x16x64_i8 v[0:3], v[158:161], v[234:237], v[0:3]
	s_setprio 0
	s_setprio 1
	v_mfma_i32_16x16x64_i8 v[62:65], v[142:145], v[196:199], 0
	v_mfma_i32_16x16x64_i8 v[58:61], v[186:189], v[196:199], 0
	v_mfma_i32_16x16x64_i8 v[46:49], v[142:145], v[208:211], 0
	v_mfma_i32_16x16x64_i8 v[42:45], v[186:189], v[208:211], 0
	v_mfma_i32_16x16x64_i8 v[28:31], v[142:145], v[216:219], 0
	v_mfma_i32_16x16x64_i8 v[24:27], v[186:189], v[216:219], 0
	v_mfma_i32_16x16x64_i8 v[12:15], v[142:145], v[230:233], 0
	v_mfma_i32_16x16x64_i8 v[8:11], v[186:189], v[230:233], 0
	v_mfma_i32_16x16x64_i8 v[62:65], v[182:185], v[204:207], v[62:65]
	v_mfma_i32_16x16x64_i8 v[58:61], v[190:193], v[204:207], v[58:61]
	v_mfma_i32_16x16x64_i8 v[46:49], v[182:185], v[212:215], v[46:49]
	v_mfma_i32_16x16x64_i8 v[42:45], v[190:193], v[212:215], v[42:45]
	v_mfma_i32_16x16x64_i8 v[28:31], v[182:185], v[226:229], v[28:31]
	v_mfma_i32_16x16x64_i8 v[24:27], v[190:193], v[226:229], v[24:27]
	v_mfma_i32_16x16x64_i8 v[12:15], v[182:185], v[234:237], v[12:15]
	v_mfma_i32_16x16x64_i8 v[8:11], v[190:193], v[234:237], v[8:11]
	s_setprio 0
	s_barrier
	ds_read_b128 v[130:133], v174
	ds_read_b128 v[134:137], v175
	ds_read_b128 v[138:141], v166
	ds_read_b128 v[142:145], v167
	ds_read_b128 v[158:161], v176
	ds_read_b128 v[182:185], v177
	ds_read_b128 v[186:189], v178
	ds_read_b128 v[190:193], v179
	s_add_u32 s42, s72, 0x20000
	s_addc_u32 s43, s73, 0
	s_mov_b32 m0, s65
	v_lshl_add_u64 v[242:243], s[42:43], 0, v[152:153]
	ds_read_b128 v[196:199], v181 offset:32768
	ds_read_b128 v[204:207], v181 offset:33792
	ds_read_b128 v[208:211], v181 offset:34816
	ds_read_b128 v[212:215], v181 offset:35840
	ds_read_b128 v[216:219], v181 offset:36864
	ds_read_b128 v[226:229], v181 offset:37888
	ds_read_b128 v[230:233], v181 offset:38912
	ds_read_b128 v[234:237], v181 offset:39936
	global_load_lds_dwordx4 v[242:243], off
	v_lshl_add_u64 v[242:243], s[42:43], 0, v[148:149]
	s_mov_b32 m0, s97
	s_nop 0
	global_load_lds_dwordx4 v[242:243], off
	s_waitcnt vmcnt(8)
	s_waitcnt lgkmcnt(0)
	s_barrier
	s_setprio 1
	s_waitcnt lgkmcnt(0)
	v_mfma_i32_16x16x64_i8 v[126:129], v[138:141], v[196:199], v[126:129]
	v_mfma_i32_16x16x64_i8 v[122:125], v[134:137], v[196:199], v[122:125]
	v_mfma_i32_16x16x64_i8 v[110:113], v[138:141], v[208:211], v[110:113]
	v_mfma_i32_16x16x64_i8 v[106:109], v[134:137], v[208:211], v[106:109]
	v_mfma_i32_16x16x64_i8 v[94:97], v[138:141], v[216:219], v[94:97]
	v_mfma_i32_16x16x64_i8 v[90:93], v[134:137], v[216:219], v[90:93]
	v_mfma_i32_16x16x64_i8 v[78:81], v[138:141], v[230:233], v[78:81]
	v_mfma_i32_16x16x64_i8 v[74:77], v[134:137], v[230:233], v[74:77]
	v_mfma_i32_16x16x64_i8 v[126:129], v[130:133], v[204:207], v[126:129]
	v_mfma_i32_16x16x64_i8 v[122:125], v[158:161], v[204:207], v[122:125]
	v_mfma_i32_16x16x64_i8 v[110:113], v[130:133], v[212:215], v[110:113]
	v_mfma_i32_16x16x64_i8 v[106:109], v[158:161], v[212:215], v[106:109]
	v_mfma_i32_16x16x64_i8 v[94:97], v[130:133], v[226:229], v[94:97]
	v_mfma_i32_16x16x64_i8 v[90:93], v[158:161], v[226:229], v[90:93]
	v_mfma_i32_16x16x64_i8 v[78:81], v[130:133], v[234:237], v[78:81]
	v_mfma_i32_16x16x64_i8 v[74:77], v[158:161], v[234:237], v[74:77]
	s_setprio 0
	s_setprio 1
	v_mfma_i32_16x16x64_i8 v[118:121], v[142:145], v[196:199], v[118:121]
	v_mfma_i32_16x16x64_i8 v[114:117], v[186:189], v[196:199], v[114:117]
	v_mfma_i32_16x16x64_i8 v[102:105], v[142:145], v[208:211], v[102:105]
	v_mfma_i32_16x16x64_i8 v[98:101], v[186:189], v[208:211], v[98:101]
	v_mfma_i32_16x16x64_i8 v[86:89], v[142:145], v[216:219], v[86:89]
	v_mfma_i32_16x16x64_i8 v[82:85], v[186:189], v[216:219], v[82:85]
	v_mfma_i32_16x16x64_i8 v[70:73], v[142:145], v[230:233], v[70:73]
	v_mfma_i32_16x16x64_i8 v[66:69], v[186:189], v[230:233], v[66:69]
	v_mfma_i32_16x16x64_i8 v[118:121], v[182:185], v[204:207], v[118:121]
	v_mfma_i32_16x16x64_i8 v[114:117], v[190:193], v[204:207], v[114:117]
	v_mfma_i32_16x16x64_i8 v[102:105], v[182:185], v[212:215], v[102:105]
	v_mfma_i32_16x16x64_i8 v[98:101], v[190:193], v[212:215], v[98:101]
	v_mfma_i32_16x16x64_i8 v[86:89], v[182:185], v[226:229], v[86:89]
	v_mfma_i32_16x16x64_i8 v[82:85], v[190:193], v[226:229], v[82:85]
	v_mfma_i32_16x16x64_i8 v[70:73], v[182:185], v[234:237], v[70:73]
	v_mfma_i32_16x16x64_i8 v[66:69], v[190:193], v[234:237], v[66:69]
	s_setprio 0
	s_barrier
; #define PG8_STAGE(bufoff, gbase, voff) do { _Pragma("unroll") for (int _i = 0; _i < 2; ++_i) \
;         __builtin_amdgcn_global_load_lds((const unsigned*)((const char*)(gbase) + (voff)[_i]), (LAS unsigned*)(lds + (bufoff) + ldsw + _i * 8192), 16, 0, 0); } while (0)
; #define PG8_STAGE_A(bufoff, h, abase) do { _Pragma("unroll") for (int _i = 0; _i < 2; ++_i) { \
;         const char* _src = GATHER ? ((const char*)(abase) + gA[h][_i]) : ((const char*)(abase) + (size_t)(h) * hstep + voffA[_i]); \
;         __builtin_amdgcn_global_load_lds((const unsigned*)_src, (LAS unsigned*)(lds + (bufoff) + ldsw + _i * 8192), 16, 0, 0); } } while (0)
; #define PG8_LDA(dst, b, h) do { _Pragma("unroll") for (int m = 0; m < 4; ++m) PG8_LD2(dst[m], PG8_SA(b, h) + aoff + m * 2048); } while (0)
; #define PG8_WAIT_V(n) asm volatile("s_waitcnt vmcnt(" #n ")" ::: "memory")
; #define PG8_WAIT_L(n) asm volatile("s_waitcnt lgkmcnt(" #n ")" ::: "memory")
; #define PG8_BAR __builtin_amdgcn_s_barrier()
; #define PG8_SCHED __builtin_amdgcn_sched_barrier(0)
; template <int DT  , class Epi, class Sched, class Hook = NoHook>
; __device__ __forceinline__ void gemm_phase(LAS unsigned char* lds, const Sched& S, const Epi& E, int wave_s, LAS unsigned char* aux  ,
;                                            const Hook& H = Hook()  ) {
;     ...
;             PG8_LDA(At, 1, 1); PG8_STAGE(PG8_SB(1, 0), b3, voffB); PG8_STAGE(PG8_SB(1, 1), b3 + hstep, voffB); PG8_STAGE_A(PG8_SA(1, 0), 0, a3);
;             PG8_WAIT_V(8); PG8_WAIT_L(0); PG8_BAR; PG8_MMA(1, 0, At, B0); PG8_MMA(1, 1, At, B1); PG8_BAR; PG8_SCHED;
;         }
	s_mov_b32 m0, s57
	v_lshl_add_u64 v[162:163], v[162:163], 0, s[58:59]
	s_add_u32 s18, s18, 0x20080
	ds_read_b128 v[196:199], v181 offset:49152
	ds_read_b128 v[204:207], v181 offset:50176
	ds_read_b128 v[208:211], v181 offset:51200
	ds_read_b128 v[212:215], v181 offset:52224
	ds_read_b128 v[216:219], v181 offset:53248
	ds_read_b128 v[226:229], v181 offset:54272
	ds_read_b128 v[230:233], v181 offset:55296
	ds_read_b128 v[234:237], v181 offset:56320
	global_load_lds_dwordx4 v[162:163], off
	v_lshl_add_u64 v[162:163], v[200:201], 0, s[58:59]
	s_mov_b32 m0, s10
	s_addc_u32 s19, s19, 0
	global_load_lds_dwordx4 v[162:163], off
	v_lshl_add_u64 v[162:163], s[18:19], 0, v[150:151]
	s_mov_b32 m0, s48
	s_nop 0
	global_load_lds_dwordx4 v[162:163], off
	v_lshl_add_u64 v[162:163], s[18:19], 0, v[146:147]
	s_mov_b32 m0, s44
	s_nop 0
	global_load_lds_dwordx4 v[162:163], off
	v_lshl_add_u64 v[162:163], v[238:239], 0, s[58:59]
	s_mov_b32 m0, s94
	s_nop 0
	global_load_lds_dwordx4 v[162:163], off
	v_lshl_add_u64 v[162:163], v[240:241], 0, s[58:59]
	s_mov_b32 m0, s95
	s_nop 0
	global_load_lds_dwordx4 v[162:163], off
	s_waitcnt vmcnt(8)
	s_waitcnt lgkmcnt(0)
	s_barrier
	s_setprio 1
	s_waitcnt lgkmcnt(0)
	v_mfma_i32_16x16x64_i8 v[54:57], v[138:141], v[196:199], v[54:57]
	v_mfma_i32_16x16x64_i8 v[50:53], v[134:137], v[196:199], v[50:53]
	v_mfma_i32_16x16x64_i8 v[38:41], v[138:141], v[208:211], v[38:41]
	v_mfma_i32_16x16x64_i8 v[34:37], v[134:137], v[208:211], v[34:37]
	v_mfma_i32_16x16x64_i8 v[20:23], v[138:141], v[216:219], v[20:23]
	v_mfma_i32_16x16x64_i8 v[16:19], v[134:137], v[216:219], v[16:19]
	v_mfma_i32_16x16x64_i8 v[4:7], v[138:141], v[230:233], v[4:7]
	v_mfma_i32_16x16x64_i8 v[0:3], v[134:137], v[230:233], v[0:3]
	v_mfma_i32_16x16x64_i8 v[54:57], v[130:133], v[204:207], v[54:57]
	v_mfma_i32_16x16x64_i8 v[50:53], v[158:161], v[204:207], v[50:53]
	v_mfma_i32_16x16x64_i8 v[38:41], v[130:133], v[212:215], v[38:41]
	v_mfma_i32_16x16x64_i8 v[34:37], v[158:161], v[212:215], v[34:37]
	v_mfma_i32_16x16x64_i8 v[20:23], v[130:133], v[226:229], v[20:23]
	v_mfma_i32_16x16x64_i8 v[16:19], v[158:161], v[226:229], v[16:19]
	v_mfma_i32_16x16x64_i8 v[4:7], v[130:133], v[234:237], v[4:7]
	v_mfma_i32_16x16x64_i8 v[0:3], v[158:161], v[234:237], v[0:3]
	s_setprio 0
	s_setprio 1
	v_mfma_i32_16x16x64_i8 v[62:65], v[142:145], v[196:199], v[62:65]
	v_mfma_i32_16x16x64_i8 v[58:61], v[186:189], v[196:199], v[58:61]
	v_mfma_i32_16x16x64_i8 v[46:49], v[142:145], v[208:211], v[46:49]
	v_mfma_i32_16x16x64_i8 v[42:45], v[186:189], v[208:211], v[42:45]
	v_mfma_i32_16x16x64_i8 v[28:31], v[142:145], v[216:219], v[28:31]
	v_mfma_i32_16x16x64_i8 v[24:27], v[186:189], v[216:219], v[24:27]
	v_mfma_i32_16x16x64_i8 v[12:15], v[142:145], v[230:233], v[12:15]
	v_mfma_i32_16x16x64_i8 v[8:11], v[186:189], v[230:233], v[8:11]
	v_mfma_i32_16x16x64_i8 v[62:65], v[182:185], v[204:207], v[62:65]
	v_mfma_i32_16x16x64_i8 v[58:61], v[190:193], v[204:207], v[58:61]
	v_mfma_i32_16x16x64_i8 v[46:49], v[182:185], v[212:215], v[46:49]
	v_mfma_i32_16x16x64_i8 v[42:45], v[190:193], v[212:215], v[42:45]
	v_mfma_i32_16x16x64_i8 v[28:31], v[182:185], v[226:229], v[28:31]
	v_mfma_i32_16x16x64_i8 v[24:27], v[190:193], v[226:229], v[24:27]
	v_mfma_i32_16x16x64_i8 v[12:15], v[182:185], v[234:237], v[12:15]
	v_mfma_i32_16x16x64_i8 v[8:11], v[190:193], v[234:237], v[8:11]
	s_setprio 0
	s_barrier
	s_add_i32 vcc_lo, vcc_lo, 2
	s_add_u32 s46, s46, 0x100
	s_addc_u32 s47, s47, 0
	s_add_u32 s76, s76, 0x100
	s_addc_u32 s77, s77, 0
	s_cmp_gt_u32 vcc_lo, 5

; __global__ void __launch_bounds__(NWAVES * 64, 2) mk_fwd(Args args) {
;     ...
;                 {   int hh = (bx >> 3) & 7; asm volatile("" : "+s"(hh));
;                     const float sl2 = exp2f(-(float)(hh + 1)) * LOG2E;
;                     for (int i = tid; i < 4 * 648; i += NWAVES * 64) { const int sft = i / 648, k = i - sft * 648; const float ad = fabsf((float)(k - sft - 320)); TAB1[i] = ad <= 64.f ? -sl2 * ad : -3.0e38f; }
.LBB0_201:
	s_mov_b32 s2, -1
	v_readlane_b32 s4, v254, 40
	s_waitcnt lgkmcnt(0)
	s_barrier
	v_readlane_b32 s5, v254, 41
	v_mbcnt_lo_u32_b32 v0, s2, 0
	v_mbcnt_hi_u32_b32 v127, s2, v0
	s_mov_b64 s[2:3], -1
	s_and_b64 vcc, exec, s[4:5]
	s_cbranch_vccz .LBB0_355
	v_readlane_b32 s2, v253, 9
	s_nop 1
	v_add_u32_e32 v0, s2, v127
	v_readlane_b32 s2, v252, 6
	s_and_b32 s2, s2, 7
	s_add_i32 s2, s2, 1
	s_nop 0
	v_cvt_f32_i32_e32 v1, s2
	s_mov_b32 s2, 0x42fc0000
	v_cmp_lt_f32_e32 vcc, s2, v1
	s_nop 1
	v_cndmask_b32_e32 v2, 0, v221, vcc
	v_sub_f32_e32 v1, v2, v1
	v_exp_f32_e32 v1, v1
	s_and_b64 s[2:3], vcc, exec
	s_cselect_b32 s2, 0xffffffc0, 0
	v_ldexp_f32 v1, v1, s2
	s_movk_i32 s2, 0xa20
	v_mul_f32_e32 v6, 0x3fb8aa3b, v1
	v_cmp_gt_i32_e32 vcc, s2, v0
	s_and_saveexec_b64 s[4:5], vcc
	s_cbranch_execz .LBB0_215
	v_max_i32_e32 v1, 0x820, v0
	v_sub_u32_e32 v1, v1, v0
	v_add_u32_e32 v1, 0x1ff, v1
	s_movk_i32 s2, 0x1ff
	v_cmp_lt_u32_e32 vcc, s2, v1
	s_mov_b64 s[2:3], -1
	v_mov_b32_e32 v2, v0
	s_and_saveexec_b64 s[6:7], vcc
	s_cbranch_execz .LBB0_212
	v_lshrrev_b32_e32 v7, 9, v1
	v_add_u32_e32 v4, -1, v7
	v_xor_b32_e32 v2, 0x80000000, v6
	v_add_u32_e32 v1, 0x200, v0
	v_lshrrev_b32_e32 v5, 1, v4
	v_mov_b32_e32 v3, v2
	v_add_u32_e32 v8, 1, v5
	v_cmp_lt_u32_e32 vcc, 5, v4
	v_mov_b32_e32 v11, 0
	v_mov_b64_e32 v[4:5], v[0:1]
	s_and_saveexec_b64 s[8:9], vcc
	s_cbranch_execz .LBB0_208
	v_readlane_b32 s2, v255, 24
	v_and_b32_e32 v9, -4, v8
	s_mov_b32 s12, 0
	v_lshl_add_u32 v10, v127, 2, s2
	s_mov_b64 s[10:11], 0
	v_mov_b64_e32 v[4:5], v[0:1]
	s_mov_b32 s13, 0x42800000
	s_mov_b32 s14, 0x1948b0fd
	s_movk_i32 s15, 0xfd78
	s_movk_i32 s16, 0xfec0
	s_movk_i32 s17, 0x2c0
	s_movk_i32 s18, 0x6c0
	s_movk_i32 s19, 0xac0

; __global__ void __launch_bounds__(NWAVES * 64, 2) mk_fwd(Args args) {
;     ...
;                 for (int bu = bx; bu < 2048; bu += G, ++bu_idx) {
;                     {   const int target = (bu_idx >= ((bx >> 3) % n_bu)) ? cv_mine : 0;
;                         for (; cv_done < target; ++cv_done, cv_it += G, cv_par ^= 1) {
;                             const int lyr = cv_first + cv_it / 1536, r = cv_it % 1536;
;                             if (r < 1024) { const int mi = lyr * 32 + (r >> 5), nb = ((r & 31) + 8 * ((r >> 6) & 3)) & 31;
;                                 q8_cols_item<true, false>(args.in[11] + (size_t)mi * D * 2048, 2048, nb * 64, ws + WS_WGU + (size_t)mi * 2048 * 1024, (float*)(ws + WS_SB) + (size_t)mi * 2048, CAM, cv_par, wave, lane); }
;                             else { const int r2 = r - 1024, mi = lyr * 32 + (r2 >> 4), nb = ((r2 & 15) + 8 * ((r2 >> 6) & 1)) & 15;
;                                 q8_cols_item<false, true>(args.in[13] + (size_t)mi * D * D, D, nb * 64, ws + WS_WDN + (size_t)mi * D * 1024, (float*)(ws + WS_SBD) + (size_t)mi * D, CAM, cv_par, wave, lane); }
;                         }
;                     }
;     ...
;                         const int ud = bu - 1024, b = ud >> 6, kvh = (ud >> 5) & 1, qb = ud & 31;
;                         const bf16_t* hb = HB + (size_t)b * SEQ * ODD_IN;
;                         const int hp = wave & 1, q0 = 64 * qb + 16 * (wave >> 1), qp = q0 + c;
;                         bf16x8 bq[2][2]; float m[2], l[2], slope2[2]; f32x4 O[2][4];
; #pragma unroll
;                         for (int j = 0; j < 2; ++j) { const int hq = 4 * kvh + 2 * hp + j; const bf16_t* qr = hb + (size_t)qp * ODD_IN + 1536 + hq * 64 + 8 * g;
;                             bq[j][0] = q_prescale(*(const bf16x8*)qr); bq[j][1] = q_prescale(*(const bf16x8*)(qr + 32)); m[j] = -1e30f; l[j] = 0.f; slope2[j] = exp2f(-(float)(hq + 1)) * LOG2E;
; #pragma unroll
;                             for (int mt = 0; mt < 4; ++mt) O[j][mt] = (f32x4){0.f, 0.f, 0.f, 0.f}; }
;                         const char* kpb = (const char*)(hb + 2048 + kvh * 64); const char* vpb = (const char*)(hb + 2176 + kvh * 64);
;                         { const float fq1[1] = {(float)qp}; const LAS unsigned char* const notab[1] = {nullptr}; attn_stream<2, 1, false>(kpb, vpb, 64 * qb - 128, 5, 128.f, fq1, notab, slope2, bq, m, l, O, sh, tid, lane, 0, 4); }
.LBB0_241:
	s_mov_b32 s99, s26
	s_cmp_lg_u32 s72, 0x100
	s_cbranch_scc1 .Lremap_done
	s_and_b32 s98, s26, 0xff
	s_lshr_b32 s99, s26, 8
	s_cmp_lt_u32 s99, 4
	s_cbranch_scc0 .Lremap_win
	s_lshr_b32 vcc_lo, s98, 6
	s_lshl_b32 s99, s99, 2
	s_add_i32 s99, s99, vcc_lo
	s_lshl_b32 s99, s99, 6
	s_and_b32 vcc_lo, s98, 7
	s_lshl_b32 vcc_lo, vcc_lo, 3
	s_add_i32 s99, s99, vcc_lo
	s_bfe_u32 vcc_lo, s98, 0x30003
	s_add_i32 s99, s99, vcc_lo
	s_branch .Lremap_done
.Lremap_win:
	s_add_i32 s99, s99, -4
	s_lshl_b32 s99, s99, 3
	s_and_b32 vcc_lo, s98, 7
	s_add_i32 s99, s99, vcc_lo
	s_lshl_b32 s99, s99, 5
	s_lshr_b32 vcc_lo, s98, 3
	s_add_i32 s99, s99, vcc_lo
	s_addk_i32 s99, 0x400
.Lremap_done:
	v_mov_b32_e32 v193, v154
	v_mov_b32_e32 v192, v155
	s_mov_b64 s[8:9], -1
	v_lshlrev_b32_e32 v130, 3, v192
	s_cmpk_gt_i32 s99, 0x3ff
	v_add_u32_e32 v196, v159, v164
	v_add_u32_e32 v197, v159, v165
	v_ashrrev_i32_e32 v131, 31, v130
	s_cbranch_scc0 .LBB0_259
	s_add_i32 s8, s99, 0xfffffc00
	s_lshr_b32 s12, s8, 6
	s_lshl_b32 s13, s99, 6
	s_and_b32 s13, s13, 0x7c0
	s_bfe_u32 s15, s99, 0x10005
	s_mul_i32 s8, s12, 0x900000
	s_mul_hi_u32 s9, s12, 0x900000
	s_add_u32 s8, s92, s8
	s_addc_u32 s9, s93, s9
	s_lshl_b32 s10, s99, 6
	s_and_b32 s18, s10, 0x7c0
	v_readlane_b32 s10, v253, 13
	s_add_i32 s10, s18, s10
	v_readlane_b32 s11, v253, 14
	v_add_u32_e32 v198, s10, v193
	s_lshl_b32 s10, s15, 2
	v_mov_b64_e32 v[0:1], s[8:9]
	s_or_b32 s14, s10, s11
	v_mad_i64_i32 v[0:1], s[10:11], v198, s50, v[0:1]
	s_or_b32 s10, s14, 1
	s_nop 0
	v_cvt_f32_ubyte0_e32 v16, s10
	s_mov_b32 s19, 0x42fc0000
	s_lshl_b32 s68, s14, 7
	s_lshl_b32 s11, s14, 6
	v_cmp_lt_f32_e32 vcc, s19, v16
	v_lshl_add_u64 v[8:9], v[130:131], 1, v[0:1]
	s_and_b64 s[16:17], vcc, exec
	v_lshl_add_u64 v[4:5], v[8:9], 0, s[68:69]
	s_cselect_b32 s16, 0xffffffc0, 0
	s_lshl_b32 s68, s10, 7
	global_load_dwordx4 v[0:3], v[4:5], off offset:3072
	s_nop 0
	global_load_dwordx4 v[4:7], v[4:5], off offset:3136
	v_lshl_add_u64 v[12:13], v[8:9], 0, s[68:69]
	global_load_dwordx4 v[8:11], v[12:13], off offset:3072
	global_load_dwordx4 v[20:23], v[12:13], off offset:3136
	v_lshl_add_u64 v[14:15], s[8:9], 0, v[124:125]
	s_add_i32 s8, s14, 2
	v_cvt_f32_ubyte0_e32 v40, s8
	v_cndmask_b32_e32 v17, 0, v221, vcc
	s_lshl_b32 s10, s10, 6
	v_cmp_lt_f32_e32 vcc, s19, v40
	s_and_b64 s[8:9], vcc, exec
	s_cselect_b32 s8, 0xffffffc0, 0
	s_addk_i32 s18, 0xff80
	s_lshl_b32 s68, s15, 7
	s_max_i32 s9, s18, 0
	v_lshl_add_u64 v[132:133], v[14:15], 0, s[68:69]
	v_or_b32_e32 v14, s9, v156
	v_sub_f32_e32 v16, v17, v16
	s_max_i32 s15, s18, 0xffffffc0
	v_mul_u32_u24_e32 v12, 0x1200, v14
	v_exp_f32_e32 v34, v16
	v_add_u32_e32 v16, s15, v160
	v_or_b32_e32 v32, v12, v157
	v_mul_i32_i24_e32 v17, 0x1200, v16
	v_lshl_add_u64 v[12:13], v[132:133], 0, v[32:33]
	v_mad_u32_u24 v32, v14, s50, v158
	v_lshl_add_u64 v[14:15], v[132:133], 0, v[32:33]
	v_or_b32_e32 v32, v17, v157
	global_load_dwordx4 v[42:45], v[12:13], off
	global_load_dwordx4 v[46:49], v[14:15], off
	v_lshl_add_u64 v[12:13], v[132:133], 0, v[32:33]
	v_mad_i32_i24 v32, v16, s50, v158
	v_lshl_add_u64 v[16:17], v[132:133], 0, v[32:33]
	global_load_dwordx4 v[12:15], v[12:13], off
	s_nop 0
	global_load_dwordx4 v[16:19], v[16:17], off
	s_mov_b32 s18, 0x3e38aa3b
	v_ldexp_f32 v32, v34, s16
	v_cndmask_b32_e32 v41, 0, v221, vcc
	v_mul_f32_e32 v136, 0xbfb8aa3b, v32
	v_mov_b32_e32 v32, v33
	s_mov_b32 s15, 0
	v_mov_b32_e32 v138, v136
	v_mov_b32_e32 v139, v136
	v_mov_b32_e32 v200, 0xf149f2ca
	v_mov_b32_e32 v201, 0xf149f2ca
	v_mov_b64_e32 v[142:143], v[32:33]
	s_waitcnt vmcnt(0)
	ds_write_b128 v196, v[42:45]
	ds_write_b128 v197, v[46:49]
	v_lshlrev_b32_e32 v24, 16, v0
	v_and_b32_e32 v25, 0xffff0000, v0
	v_lshlrev_b32_e32 v0, 16, v1
	v_and_b32_e32 v1, 0xffff0000, v1
	v_pk_mul_f32 v[24:25], v[24:25], s[18:19] op_sel_hi:[1,0]
	v_pk_mul_f32 v[0:1], v[0:1], s[18:19] op_sel_hi:[1,0]
	v_cvt_pk_bf16_f32 v24, v24, v25
	v_cvt_pk_bf16_f32 v25, v0, v1
	v_lshlrev_b32_e32 v0, 16, v8
	v_and_b32_e32 v1, 0xffff0000, v8
	v_pk_mul_f32 v[0:1], v[0:1], s[18:19] op_sel_hi:[1,0]
	v_lshlrev_b32_e32 v26, 16, v2
	v_cvt_pk_bf16_f32 v34, v0, v1
	v_lshlrev_b32_e32 v0, 16, v20
	v_and_b32_e32 v1, 0xffff0000, v20
	v_pk_mul_f32 v[0:1], v[0:1], s[18:19] op_sel_hi:[1,0]
	v_and_b32_e32 v27, 0xffff0000, v2
	v_cvt_pk_bf16_f32 v38, v0, v1
	v_sub_f32_e32 v0, v41, v40
	v_exp_f32_e32 v0, v0
	v_cvt_f32_i32_e32 v1, v198
	v_lshlrev_b32_e32 v2, 16, v3
	v_and_b32_e32 v3, 0xffff0000, v3
	v_lshlrev_b32_e32 v28, 16, v4
	v_and_b32_e32 v29, 0xffff0000, v4
	v_lshlrev_b32_e32 v4, 16, v5
	v_and_b32_e32 v5, 0xffff0000, v5
	v_lshlrev_b32_e32 v30, 16, v6
	v_and_b32_e32 v31, 0xffff0000, v6
	v_lshlrev_b32_e32 v6, 16, v7
	v_and_b32_e32 v7, 0xffff0000, v7
	v_pk_mul_f32 v[26:27], v[26:27], s[18:19] op_sel_hi:[1,0]
	v_pk_mul_f32 v[2:3], v[2:3], s[18:19] op_sel_hi:[1,0]
	v_pk_mul_f32 v[28:29], v[28:29], s[18:19] op_sel_hi:[1,0]
	v_pk_mul_f32 v[4:5], v[4:5], s[18:19] op_sel_hi:[1,0]
	v_pk_mul_f32 v[30:31], v[30:31], s[18:19] op_sel_hi:[1,0]
	v_pk_mul_f32 v[6:7], v[6:7], s[18:19] op_sel_hi:[1,0]
	v_cvt_pk_bf16_f32 v26, v26, v27
	v_cvt_pk_bf16_f32 v27, v2, v3
	v_lshlrev_b32_e32 v2, 16, v9
	v_and_b32_e32 v3, 0xffff0000, v9
	v_ldexp_f32 v0, v0, s8
	v_cvt_pk_bf16_f32 v28, v28, v29
	v_cvt_pk_bf16_f32 v29, v4, v5
	v_cvt_pk_bf16_f32 v30, v30, v31
	v_cvt_pk_bf16_f32 v31, v6, v7
	v_pk_mul_f32 v[2:3], v[2:3], s[18:19] op_sel_hi:[1,0]
	v_lshlrev_b32_e32 v4, 16, v10
	v_and_b32_e32 v5, 0xffff0000, v10
	v_lshlrev_b32_e32 v6, 16, v11
	v_and_b32_e32 v7, 0xffff0000, v11
	v_mul_f32_e32 v134, 0xbfb8aa3b, v0
	v_cvt_i32_f32_e32 v0, v1
	v_pk_mul_f32 v[4:5], v[4:5], s[18:19] op_sel_hi:[1,0]
	v_pk_mul_f32 v[6:7], v[6:7], s[18:19] op_sel_hi:[1,0]
	v_cvt_pk_bf16_f32 v35, v2, v3
	v_lshlrev_b32_e32 v2, 16, v21
	v_and_b32_e32 v3, 0xffff0000, v21
	v_cvt_pk_bf16_f32 v36, v4, v5
	v_cvt_pk_bf16_f32 v37, v6, v7
	v_pk_mul_f32 v[2:3], v[2:3], s[18:19] op_sel_hi:[1,0]
	v_lshlrev_b32_e32 v4, 16, v22
	v_and_b32_e32 v5, 0xffff0000, v22
	v_lshlrev_b32_e32 v6, 16, v23
	v_and_b32_e32 v7, 0xffff0000, v23
	v_pk_mul_f32 v[4:5], v[4:5], s[18:19] op_sel_hi:[1,0]
	v_pk_mul_f32 v[6:7], v[6:7], s[18:19] op_sel_hi:[1,0]
	v_cvt_pk_bf16_f32 v39, v2, v3
	v_mov_b32_e32 v2, v33
	v_mov_b32_e32 v3, v33
	v_cvt_pk_bf16_f32 v40, v4, v5
	v_cvt_pk_bf16_f32 v41, v6, v7
	v_sub_u32_e32 v199, v186, v0
	v_mov_b32_e32 v0, v33
	v_mov_b32_e32 v1, v33
	v_mov_b64_e32 v[6:7], v[2:3]
	v_mov_b64_e32 v[10:11], v[2:3]
	v_mov_b64_e32 v[22:23], v[2:3]
	v_mov_b64_e32 v[44:45], v[2:3]
	v_mov_b64_e32 v[48:49], v[2:3]
	v_mov_b64_e32 v[52:53], v[2:3]
	v_mov_b64_e32 v[56:57], v[2:3]
	v_mov_b32_e32 v140, v134
	v_mov_b32_e32 v141, v134
	v_mov_b64_e32 v[4:5], v[0:1]
	v_mov_b64_e32 v[8:9], v[0:1]
	v_mov_b64_e32 v[20:21], v[0:1]
	v_mov_b64_e32 v[42:43], v[0:1]
	v_mov_b64_e32 v[46:47], v[0:1]
	v_mov_b64_e32 v[50:51], v[0:1]
	v_mov_b64_e32 v[54:55], v[0:1]
	s_waitcnt lgkmcnt(0)
	s_barrier
	s_branch .LBB0_246

; __global__ void __launch_bounds__(NWAVES * 64, 2) mk_fwd(Args args) {
;     ...
;                     if (bu < 1024) {
;                         const int b = bu >> 6, h = (bu >> 3) & 7, ib = bu & 7;
;                         const bf16_t* hb = HB + (size_t)b * SEQ * ODD_IN;
;                         const char* kpb = (const char*)(hb + 512 + h * 64); const char* vpb = (const char*)(hb + 1024 + h * 64);
;                         const float slope2[1] = {exp2f(-(float)(h + 1)) * LOG2E};
;                         bf16x8 bq[2][2]; float m[2], l[2], fq2[2]; f32x4 O[2][4];
;                         auto per_wave_part = [&](auto RR) { constexpr int rr = decltype(RR)::value;
;                             const int rho = wave + 8 * rr, q0 = rho + 256 * ib, qp = q0 + 16 * c;
;                             bf16x8 bq1[1][2];
;                             { const bf16_t* qr = hb + (size_t)qp * ODD_IN + h * 64 + 8 * g; bq1[0][0] = q_prescale(*(const bf16x8*)qr); bq1[0][1] = q_prescale(*(const bf16x8*)(qr + 32)); }
.LBB0_259:
	s_and_b64 vcc, exec, s[8:9]
	s_cbranch_vccz .LBB0_230
	s_ashr_i32 s28, s99, 6
	s_and_b32 s14, s99, 7
	s_mul_i32 s9, s28, 0x900000
	s_mul_hi_i32 s8, s28, 0x900000
	s_add_u32 s10, s92, s9
	s_addc_u32 s11, s93, s8
	s_lshl_b32 s8, s99, 3
	s_and_b32 s8, s8, 0x1c0
	s_lshl_b32 s68, s8, 1
	s_add_u32 s8, s10, s68
	v_lshlrev_b32_e32 v132, 4, v193
	s_addc_u32 s9, s11, 0
	s_lshl_b32 s29, s14, 8
	v_add_u32_e32 v117, s73, v132
	v_add_u32_e32 v2, s29, v117
	v_mov_b64_e32 v[0:1], s[10:11]
	v_mad_i64_i32 v[0:1], s[12:13], v2, s50, v[0:1]
	v_lshl_add_u64 v[0:1], v[0:1], 0, s[68:69]
	v_lshl_add_u64 v[4:5], v[130:131], 1, v[0:1]
	global_load_dwordx4 v[0:3], v[4:5], off
	s_nop 0
	global_load_dwordx4 v[4:7], v[4:5], off offset:64
	s_cmp_lt_u32 s14, 6
	s_cselect_b64 s[12:13], -1, 0
	s_cmp_gt_u32 s14, 5
	s_mov_b32 s15, s73
	s_cbranch_scc1 .LBB0_262
	v_add_u32_e32 v8, s15, v166
	v_mad_u64_u32 v[8:9], s[16:17], v8, s50, v[126:127]
	v_add_u32_e32 v9, 64, v8
	global_load_dwordx4 v[40:43], v8, s[8:9] offset:1024
	global_load_dwordx4 v[24:27], v9, s[8:9] offset:1024
	v_add_u32_e32 v8, s15, v167
	v_mad_u64_u32 v[8:9], s[16:17], v8, s50, v[126:127]
	v_add_u32_e32 v9, 64, v8
	global_load_dwordx4 v[36:39], v8, s[8:9] offset:1024
	global_load_dwordx4 v[28:31], v9, s[8:9] offset:1024
	v_add_u32_e32 v8, s15, v168
	v_add_u32_e32 v9, s15, v169
	v_add_u32_e32 v12, s15, v170
	v_add_u32_e32 v13, s15, v171
	v_mul_lo_u32 v8, v8, s50
	v_mul_lo_u32 v9, v9, s50
	v_mul_lo_u32 v12, v12, s50
	v_mul_lo_u32 v13, v13, s50
	v_or_b32_e32 v8, v8, v157
	v_or_b32_e32 v9, v9, v157
	v_or_b32_e32 v12, v12, v157
	v_or_b32_e32 v20, v13, v157
	global_load_dwordx4 v[16:19], v8, s[8:9] offset:2048
	s_nop 0
	global_load_dwordx4 v[8:11], v9, s[8:9] offset:2048
	s_nop 0
	global_load_dwordx4 v[12:15], v12, s[8:9] offset:2048
	s_nop 0
	global_load_dwordx4 v[20:23], v20, s[8:9] offset:2048
	s_branch .LBB0_263

; #define LAS __attribute__((address_space(3)))
; template <int O> __device__ __forceinline__ float xor_sw(float v) { return __int_as_float(__builtin_amdgcn_ds_swizzle(__float_as_int(v), 0x1f | (O << 10))); }
; __device__ __forceinline__ float sum_x32(float v) { const auto r = __builtin_amdgcn_permlane32_swap(__float_as_uint(v), __float_as_uint(v), false, false); return __uint_as_float(r[0]) + __uint_as_float(r[1]); }
; __global__ void __launch_bounds__(NWAVES * 64, 2) mk_fwd(Args args) {
;     ...
;                         bf16x8 qraw[2][2];
; #pragma unroll
;                         for (int sl = 0; sl < 2; ++sl) { const bf16_t* qr = hb + (size_t)(256 * ib + 32 * wave + 16 * sl + c) * ODD_IN + h * 64 + 8 * g; qraw[sl][0] = *(const bf16x8*)qr; qraw[sl][1] = *(const bf16x8*)(qr + 32); }
;                         __syncthreads();
;                         {   LAS float* PARK = (LAS float*)lds;
; #pragma unroll
;                             for (int q = 0; q < 2; ++q) { float lt = l[q]; lt += xor_sw<16>(lt); lt = sum_x32(lt);
;                                 const int pp = wave + 8 * q + 16 * c;
; #pragma unroll
;                                 for (int mt = 0; mt < 4; ++mt) *(LAS f32x4*)(PARK + pp * 68 + 4 * ((4 * mt + g) ^ c)) = O[q][mt];
;                                 if (g == 0) { PARK[pp * 68 + 64] = m[q]; PARK[pp * 68 + 65] = lt; } }
;                             const LAS unsigned char* t1[2];
; #pragma unroll
;                             for (int sl = 0; sl < 2; ++sl) { const int qp = 256 * ib + 32 * wave + 16 * sl + c;
;                                 bq[sl][0] = q_prescale(qraw[sl][0]); bq[sl][1] = q_prescale(qraw[sl][1]);
;                                 m[sl] = -1e30f; l[sl] = 0.f; fq2[sl] = (float)qp;
; #pragma unroll
;                                 for (int mt = 0; mt < 4; ++mt) O[sl][mt] = (f32x4){0.f, 0.f, 0.f, 0.f};
;                                 t1[sl] = (const LAS unsigned char*)TAB1 + 2592 * (c & 3) + 4 * (320 + (c & 3) + 4 * g - qp); }
;                             attn_stream<2, 2, true>(kpb, vpb, 256 * ib - 64, 6, 64.f, fq2, t1, slope22, bq, m, l, O, sh, tid, lane, wave >> 1, (wave >> 1) + 2);
.LBB0_315:
	s_and_b32 s10, s99, 7
	s_lshl_b32 s17, s10, 8
	v_readlane_b32 s10, v253, 17
	s_or_b32 s18, s10, s17
	v_sub_u32_e32 v32, v121, v132
	v_readlane_b32 s10, v255, 26
	ds_write_b128 v187, v[108:111]
	ds_write_b128 v188, v[100:103]
	ds_write_b128 v189, v[104:107]
	ds_write_b128 v190, v[112:115]
	v_add_u32_e32 v35, s10, v32
	v_readlane_b32 s10, v255, 27
	s_mov_b32 s19, 0
	s_nop 0
	v_add_u32_e32 v108, s10, v32
	s_branch .LBB0_317

; #define PG8_LDA(dst, b, h) do { _Pragma("unroll") for (int m = 0; m < 4; ++m) PG8_LD2(dst[m], PG8_SA(b, h) + aoff + m * 2048); } while (0)
; #define PG8_BAR __builtin_amdgcn_s_barrier()
; template <int DT  , class Epi, class Sched, class Hook = NoHook>
; __device__ __forceinline__ void gemm_phase(LAS unsigned char* lds, const Sched& S, const Epi& E, int wave_s, LAS unsigned char* aux  ,
;                                            const Hook& H = Hook()  ) {
;     ...
;         for (int t = 0; t < nt; t += 2) {
;             const bool last = (t == nt - 2);
;             const char* a1 = cA + (size_t)(t + 1) * kstep;
;             const char* a2 = last ? nA : cA + (size_t)(t + 2) * kstep; const char* b2 = last ? nB : cB + (size_t)(t + 2) * kstep;
;             const char* a3 = a2 + kstep; const char* b3 = b2 + kstep;
;             PG8_LDB(B0, 0, 0); PG8_LDB(B1, 0, 1); PG8_SCHED; PG8_LDA(At, 0, 0); PG8_STAGE_A(PG8_SA(1, 1), 1, a1);
;             if (GATHER) { if (last && has_next) S.gather_lds(nxt, gA, tid, aux + ((ui + 1) & 1) * 1024); }
;             PG8_WAIT_V(8); PG8_WAIT_L(0); PG8_BAR; PG8_MMA(0, 0, At, B0); PG8_MMA(0, 1, At, B1); PG8_BAR; PG8_SCHED;
;             PG8_LDA(At, 0, 1); PG8_STAGE(PG8_SB(0, 0), b2, voffB); PG8_STAGE(PG8_SB(0, 1), b2 + hstep, voffB); PG8_STAGE_A(PG8_SA(0, 0), 0, a2);
;             PG8_WAIT_V(8); PG8_WAIT_L(0); PG8_BAR; PG8_MMA(1, 0, At, B0); PG8_MMA(1, 1, At, B1); PG8_BAR; PG8_SCHED;
;             PG8_LDB(B0, 1, 0); PG8_LDB(B1, 1, 1); PG8_SCHED; PG8_LDA(At, 1, 0); PG8_STAGE_A(PG8_SA(0, 1), 1, a2);
;             PG8_WAIT_V(8); PG8_WAIT_L(0); PG8_BAR; PG8_MMA(0, 0, At, B0); PG8_MMA(0, 1, At, B1); PG8_BAR; PG8_SCHED;
;             PG8_LDA(At, 1, 1); PG8_STAGE(PG8_SB(1, 0), b3, voffB); PG8_STAGE(PG8_SB(1, 1), b3 + hstep, voffB); PG8_STAGE_A(PG8_SA(1, 0), 0, a3);
;             PG8_WAIT_V(8); PG8_WAIT_L(0); PG8_BAR; PG8_MMA(1, 0, At, B0); PG8_MMA(1, 1, At, B1); PG8_BAR; PG8_SCHED;
;         }
;         if (wr == 0) PG8_BAR;
;         E(acc, cur, wr, wc, fr, fq, aux + 2048 + (ui & 1) * 3072);
;         H(ui);
;         if (!has_next) break;
; #pragma unroll
;         for (int a = 0; a < 2; ++a)
; #pragma unroll
;             for (int b = 0; b < 2; ++b)
; #pragma unroll
;                 for (int m = 0; m < 4; ++m)
; #pragma unroll
;                     for (int n = 0; n < 2; ++n) acc[a][b][m][n] = (acc_t){0, 0, 0, 0};
.LBB0_427:
	s_ashr_i32 s11, s10, 31
	s_lshl_b64 s[12:13], s[10:11], 19
	s_add_u32 s12, s80, s12
	s_addc_u32 s13, s81, s13
	s_and_b64 s[14:15], s[2:3], exec
	s_cselect_b32 s11, s13, s17
	s_cselect_b32 s51, s12, s16
	s_ashr_i32 s9, s8, 31
	s_lshl_b64 s[14:15], s[8:9], 19
	s_add_u32 s14, s22, s14
	s_addc_u32 s15, s23, s15
	s_and_b64 s[20:21], s[2:3], exec
	s_cselect_b32 s9, s15, s19
	s_cselect_b32 s57, s14, s18
	s_add_u32 s16, s16, 0x40080
	s_addc_u32 s17, s17, 0
	s_add_u32 s65, s18, 0x100
	s_addc_u32 s67, s19, 0
	s_mov_b32 s68, -2
	ds_read_b128 v[130:133], v180
	ds_read_b128 v[134:137], v181
	ds_read_b128 v[138:141], v176
	ds_read_b128 v[142:145], v177
	ds_read_b128 v[146:149], v182
	ds_read_b128 v[150:153], v183
	ds_read_b128 v[164:167], v184
	ds_read_b128 v[168:171], v185
	s_add_u32 s18, s16, 0xfffc0080
	s_addc_u32 s19, s17, -1
	s_cmp_eq_u32 s68, 12
	s_cselect_b32 s21, s11, s19
	s_cselect_b32 s20, s51, s18
	s_cselect_b32 s19, s9, s67
	s_cselect_b32 s18, s57, s65
	v_lshl_add_u64 v[200:201], s[16:17], 0, v[160:161]
	s_add_i32 m0, s24, 0xc000
	ds_read_b128 v[172:175], v192
	ds_read_b128 v[196:199], v192 offset:1024
	ds_read_b128 v[204:207], v192 offset:2048
	ds_read_b128 v[208:211], v192 offset:3072
	ds_read_b128 v[212:215], v192 offset:4096
	ds_read_b128 v[216:219], v192 offset:5120
	ds_read_b128 v[226:229], v192 offset:6144
	ds_read_b128 v[230:233], v192 offset:7168
	global_load_lds_dwordx4 v[200:201], off
	v_lshl_add_u64 v[200:201], s[16:17], 0, v[162:163]
	s_add_i32 m0, s24, 0xe000
	s_nop 0
	global_load_lds_dwordx4 v[200:201], off
	s_waitcnt vmcnt(8)
	s_waitcnt lgkmcnt(0)
	s_barrier
	s_setprio 1
	s_waitcnt lgkmcnt(0)
	v_mfma_f32_16x16x32_bf16 v[126:129], v[138:141], v[172:175], 0
	v_mfma_f32_16x16x32_bf16 v[122:125], v[134:137], v[172:175], 0
	v_mfma_f32_16x16x32_bf16 v[110:113], v[138:141], v[204:207], 0
	v_mfma_f32_16x16x32_bf16 v[106:109], v[134:137], v[204:207], 0
	v_mfma_f32_16x16x32_bf16 v[94:97], v[138:141], v[212:215], 0
	v_mfma_f32_16x16x32_bf16 v[90:93], v[134:137], v[212:215], 0
	v_mfma_f32_16x16x32_bf16 v[86:89], v[138:141], v[226:229], 0
	v_mfma_f32_16x16x32_bf16 v[78:81], v[134:137], v[226:229], 0
	v_mfma_f32_16x16x32_bf16 v[126:129], v[130:133], v[196:199], v[126:129]
	v_mfma_f32_16x16x32_bf16 v[122:125], v[146:149], v[196:199], v[122:125]
	v_mfma_f32_16x16x32_bf16 v[110:113], v[130:133], v[208:211], v[110:113]
	v_mfma_f32_16x16x32_bf16 v[106:109], v[146:149], v[208:211], v[106:109]
	v_mfma_f32_16x16x32_bf16 v[94:97], v[130:133], v[216:219], v[94:97]
	v_mfma_f32_16x16x32_bf16 v[90:93], v[146:149], v[216:219], v[90:93]
	v_mfma_f32_16x16x32_bf16 v[86:89], v[130:133], v[230:233], v[86:89]
	v_mfma_f32_16x16x32_bf16 v[78:81], v[146:149], v[230:233], v[78:81]
	s_setprio 0
	s_setprio 1
	v_mfma_f32_16x16x32_bf16 v[118:121], v[142:145], v[172:175], 0
	v_mfma_f32_16x16x32_bf16 v[114:117], v[164:167], v[172:175], 0
	v_mfma_f32_16x16x32_bf16 v[102:105], v[142:145], v[204:207], 0
	v_mfma_f32_16x16x32_bf16 v[98:101], v[164:167], v[204:207], 0
	v_mfma_f32_16x16x32_bf16 v[82:85], v[142:145], v[212:215], 0
	v_mfma_f32_16x16x32_bf16 v[74:77], v[164:167], v[212:215], 0
	v_mfma_f32_16x16x32_bf16 v[70:73], v[142:145], v[226:229], 0
	v_mfma_f32_16x16x32_bf16 v[66:69], v[164:167], v[226:229], 0
	v_mfma_f32_16x16x32_bf16 v[118:121], v[150:153], v[196:199], v[118:121]
	v_mfma_f32_16x16x32_bf16 v[114:117], v[168:171], v[196:199], v[114:117]
	v_mfma_f32_16x16x32_bf16 v[102:105], v[150:153], v[208:211], v[102:105]
	v_mfma_f32_16x16x32_bf16 v[98:101], v[168:171], v[208:211], v[98:101]
	v_mfma_f32_16x16x32_bf16 v[82:85], v[150:153], v[216:219], v[82:85]
	v_mfma_f32_16x16x32_bf16 v[74:77], v[168:171], v[216:219], v[74:77]
	v_mfma_f32_16x16x32_bf16 v[70:73], v[150:153], v[230:233], v[70:73]
	v_mfma_f32_16x16x32_bf16 v[66:69], v[168:171], v[230:233], v[66:69]
	s_setprio 0
	s_barrier
	s_mov_b32 m0, s25
	v_lshl_add_u64 v[200:201], s[18:19], 0, v[32:33]
	s_add_u32 s42, s18, 0x40000
	ds_read_b128 v[172:175], v192 offset:16384
	ds_read_b128 v[196:199], v192 offset:17408
	ds_read_b128 v[204:207], v192 offset:18432
	ds_read_b128 v[208:211], v192 offset:19456
	ds_read_b128 v[212:215], v192 offset:20480
	ds_read_b128 v[216:219], v192 offset:21504
	ds_read_b128 v[226:229], v192 offset:22528
	ds_read_b128 v[230:233], v192 offset:23552
	global_load_lds_dwordx4 v[200:201], off
	v_lshl_add_u64 v[234:235], s[18:19], 0, v[154:155]
	s_mov_b32 m0, s26
	s_addc_u32 s43, s19, 0
	global_load_lds_dwordx4 v[234:235], off
	v_lshl_add_u64 v[236:237], s[42:43], 0, v[32:33]
	s_mov_b32 m0, s27
	v_lshl_add_u64 v[238:239], s[20:21], 0, v[156:157]
	global_load_lds_dwordx4 v[236:237], off
	v_lshl_add_u64 v[236:237], s[42:43], 0, v[154:155]
	s_mov_b32 m0, s28
	s_nop 0
	global_load_lds_dwordx4 v[236:237], off
	v_lshl_add_u64 v[236:237], s[20:21], 0, v[158:159]
	s_mov_b32 m0, s24
	s_nop 0
	global_load_lds_dwordx4 v[236:237], off
	s_mov_b32 m0, s29
	s_nop 0
	global_load_lds_dwordx4 v[238:239], off
	s_waitcnt vmcnt(8)
	s_waitcnt lgkmcnt(0)
	s_barrier
; #define PG8_STAGE_A(bufoff, h, abase) do { _Pragma("unroll") for (int _i = 0; _i < 2; ++_i) { \
;         const char* _src = GATHER ? ((const char*)(abase) + gA[h][_i]) : ((const char*)(abase) + (size_t)(h) * hstep + voffA[_i]); \
;         __builtin_amdgcn_global_load_lds((const unsigned*)_src, (LAS unsigned*)(lds + (bufoff) + ldsw + _i * 8192), 16, 0, 0); } } while (0)
; #define PG8_LDA(dst, b, h) do { _Pragma("unroll") for (int m = 0; m < 4; ++m) PG8_LD2(dst[m], PG8_SA(b, h) + aoff + m * 2048); } while (0)
; #define PG8_LDB(dst, b, h) do { _Pragma("unroll") for (int n = 0; n < 2; ++n) PG8_LD2(dst[n], PG8_SB(b, h) + boff + n * 2048); } while (0)
; #define PG8_WAIT_V(n) asm volatile("s_waitcnt vmcnt(" #n ")" ::: "memory")
; #define PG8_WAIT_L(n) asm volatile("s_waitcnt lgkmcnt(" #n ")" ::: "memory")
; #define PG8_BAR __builtin_amdgcn_s_barrier()
; #define PG8_SCHED __builtin_amdgcn_sched_barrier(0)
; template <int DT  , class Epi, class Sched, class Hook = NoHook>
; __device__ __forceinline__ void gemm_phase(LAS unsigned char* lds, const Sched& S, const Epi& E, int wave_s, LAS unsigned char* aux  ,
;                                            const Hook& H = Hook()  ) {
;     ...
;             PG8_WAIT_V(8); PG8_WAIT_L(0); PG8_BAR; PG8_MMA(1, 0, At, B0); PG8_MMA(1, 1, At, B1); PG8_BAR; PG8_SCHED;
;             PG8_LDB(B0, 1, 0); PG8_LDB(B1, 1, 1); PG8_SCHED; PG8_LDA(At, 1, 0); PG8_STAGE_A(PG8_SA(0, 1), 1, a2);
;             PG8_WAIT_V(8); PG8_WAIT_L(0); PG8_BAR; PG8_MMA(0, 0, At, B0); PG8_MMA(0, 1, At, B1); PG8_BAR; PG8_SCHED;
	s_setprio 1
	s_waitcnt lgkmcnt(0)
	v_mfma_f32_16x16x32_bf16 v[54:57], v[138:141], v[172:175], 0
	v_mfma_f32_16x16x32_bf16 v[50:53], v[134:137], v[172:175], 0
	v_mfma_f32_16x16x32_bf16 v[38:41], v[138:141], v[204:207], 0
	v_mfma_f32_16x16x32_bf16 v[34:37], v[134:137], v[204:207], 0
	v_mfma_f32_16x16x32_bf16 v[20:23], v[138:141], v[212:215], 0
	v_mfma_f32_16x16x32_bf16 v[8:11], v[134:137], v[212:215], 0
	v_mfma_f32_16x16x32_bf16 v[4:7], v[138:141], v[226:229], 0
	v_mfma_f32_16x16x32_bf16 v[0:3], v[134:137], v[226:229], 0
	v_mfma_f32_16x16x32_bf16 v[54:57], v[130:133], v[196:199], v[54:57]
	v_mfma_f32_16x16x32_bf16 v[50:53], v[146:149], v[196:199], v[50:53]
	v_mfma_f32_16x16x32_bf16 v[38:41], v[130:133], v[208:211], v[38:41]
	v_mfma_f32_16x16x32_bf16 v[34:37], v[146:149], v[208:211], v[34:37]
	v_mfma_f32_16x16x32_bf16 v[20:23], v[130:133], v[216:219], v[20:23]
	v_mfma_f32_16x16x32_bf16 v[8:11], v[146:149], v[216:219], v[8:11]
	v_mfma_f32_16x16x32_bf16 v[4:7], v[130:133], v[230:233], v[4:7]
	v_mfma_f32_16x16x32_bf16 v[0:3], v[146:149], v[230:233], v[0:3]
	s_setprio 0
	s_setprio 1
	v_mfma_f32_16x16x32_bf16 v[58:61], v[142:145], v[172:175], 0
	v_mfma_f32_16x16x32_bf16 v[62:65], v[164:167], v[172:175], 0
	v_mfma_f32_16x16x32_bf16 v[42:45], v[142:145], v[204:207], 0
	v_mfma_f32_16x16x32_bf16 v[46:49], v[164:167], v[204:207], 0
	v_mfma_f32_16x16x32_bf16 v[24:27], v[142:145], v[212:215], 0
	v_mfma_f32_16x16x32_bf16 v[28:31], v[164:167], v[212:215], 0
	v_mfma_f32_16x16x32_bf16 v[12:15], v[142:145], v[226:229], 0
	v_mfma_f32_16x16x32_bf16 v[16:19], v[164:167], v[226:229], 0
	v_mfma_f32_16x16x32_bf16 v[58:61], v[150:153], v[196:199], v[58:61]
	v_mfma_f32_16x16x32_bf16 v[62:65], v[168:171], v[196:199], v[62:65]
	v_mfma_f32_16x16x32_bf16 v[42:45], v[150:153], v[208:211], v[42:45]
	v_mfma_f32_16x16x32_bf16 v[46:49], v[168:171], v[208:211], v[46:49]
	v_mfma_f32_16x16x32_bf16 v[24:27], v[150:153], v[216:219], v[24:27]
	v_mfma_f32_16x16x32_bf16 v[28:31], v[168:171], v[216:219], v[28:31]
	v_mfma_f32_16x16x32_bf16 v[12:15], v[150:153], v[230:233], v[12:15]
	v_mfma_f32_16x16x32_bf16 v[16:19], v[168:171], v[230:233], v[16:19]
	s_setprio 0
	s_barrier
	ds_read_b128 v[130:133], v186
	ds_read_b128 v[134:137], v187
	ds_read_b128 v[138:141], v178
	ds_read_b128 v[142:145], v179
	ds_read_b128 v[146:149], v188
	ds_read_b128 v[150:153], v189
	ds_read_b128 v[164:167], v190
	ds_read_b128 v[168:171], v191
	s_add_u32 s20, s20, 0x40000
	s_addc_u32 s21, s21, 0
	s_mov_b32 m0, s30
	v_lshl_add_u64 v[240:241], s[20:21], 0, v[158:159]
	ds_read_b128 v[172:175], v192 offset:32768
	ds_read_b128 v[196:199], v192 offset:33792
	ds_read_b128 v[204:207], v192 offset:34816
	ds_read_b128 v[208:211], v192 offset:35840
	ds_read_b128 v[212:215], v192 offset:36864
	ds_read_b128 v[216:219], v192 offset:37888
	ds_read_b128 v[226:229], v192 offset:38912
	ds_read_b128 v[230:233], v192 offset:39936
	global_load_lds_dwordx4 v[240:241], off
	v_lshl_add_u64 v[240:241], s[20:21], 0, v[156:157]
	s_mov_b32 m0, s31
	s_nop 0
	global_load_lds_dwordx4 v[240:241], off
	s_waitcnt vmcnt(8)
	s_waitcnt lgkmcnt(0)
	s_barrier
	s_setprio 1
	s_waitcnt lgkmcnt(0)
	v_mfma_f32_16x16x32_bf16 v[126:129], v[138:141], v[172:175], v[126:129]
	v_mfma_f32_16x16x32_bf16 v[122:125], v[134:137], v[172:175], v[122:125]
	v_mfma_f32_16x16x32_bf16 v[110:113], v[138:141], v[204:207], v[110:113]
	v_mfma_f32_16x16x32_bf16 v[106:109], v[134:137], v[204:207], v[106:109]
	v_mfma_f32_16x16x32_bf16 v[94:97], v[138:141], v[212:215], v[94:97]
	v_mfma_f32_16x16x32_bf16 v[90:93], v[134:137], v[212:215], v[90:93]
	v_mfma_f32_16x16x32_bf16 v[86:89], v[138:141], v[226:229], v[86:89]
	v_mfma_f32_16x16x32_bf16 v[78:81], v[134:137], v[226:229], v[78:81]
	v_mfma_f32_16x16x32_bf16 v[126:129], v[130:133], v[196:199], v[126:129]
	v_mfma_f32_16x16x32_bf16 v[122:125], v[146:149], v[196:199], v[122:125]
	v_mfma_f32_16x16x32_bf16 v[110:113], v[130:133], v[208:211], v[110:113]
	v_mfma_f32_16x16x32_bf16 v[106:109], v[146:149], v[208:211], v[106:109]
	v_mfma_f32_16x16x32_bf16 v[94:97], v[130:133], v[216:219], v[94:97]
	v_mfma_f32_16x16x32_bf16 v[90:93], v[146:149], v[216:219], v[90:93]
	v_mfma_f32_16x16x32_bf16 v[86:89], v[130:133], v[230:233], v[86:89]
	v_mfma_f32_16x16x32_bf16 v[78:81], v[146:149], v[230:233], v[78:81]
	s_setprio 0
	s_setprio 1
	v_mfma_f32_16x16x32_bf16 v[118:121], v[142:145], v[172:175], v[118:121]
	v_mfma_f32_16x16x32_bf16 v[114:117], v[164:167], v[172:175], v[114:117]
	v_mfma_f32_16x16x32_bf16 v[102:105], v[142:145], v[204:207], v[102:105]
	v_mfma_f32_16x16x32_bf16 v[98:101], v[164:167], v[204:207], v[98:101]
	v_mfma_f32_16x16x32_bf16 v[82:85], v[142:145], v[212:215], v[82:85]
	v_mfma_f32_16x16x32_bf16 v[74:77], v[164:167], v[212:215], v[74:77]
	v_mfma_f32_16x16x32_bf16 v[70:73], v[142:145], v[226:229], v[70:73]
	v_mfma_f32_16x16x32_bf16 v[66:69], v[164:167], v[226:229], v[66:69]
	v_mfma_f32_16x16x32_bf16 v[118:121], v[150:153], v[196:199], v[118:121]
	v_mfma_f32_16x16x32_bf16 v[114:117], v[168:171], v[196:199], v[114:117]
	v_mfma_f32_16x16x32_bf16 v[102:105], v[150:153], v[208:211], v[102:105]
	v_mfma_f32_16x16x32_bf16 v[98:101], v[168:171], v[208:211], v[98:101]
	v_mfma_f32_16x16x32_bf16 v[82:85], v[150:153], v[216:219], v[82:85]
	v_mfma_f32_16x16x32_bf16 v[74:77], v[168:171], v[216:219], v[74:77]
	v_mfma_f32_16x16x32_bf16 v[70:73], v[150:153], v[230:233], v[70:73]
	v_mfma_f32_16x16x32_bf16 v[66:69], v[168:171], v[230:233], v[66:69]
	s_setprio 0
	s_barrier
; #define PG8_STAGE(bufoff, gbase, voff) do { _Pragma("unroll") for (int _i = 0; _i < 2; ++_i) \
;         __builtin_amdgcn_global_load_lds((const unsigned*)((const char*)(gbase) + (voff)[_i]), (LAS unsigned*)(lds + (bufoff) + ldsw + _i * 8192), 16, 0, 0); } while (0)
; #define PG8_STAGE_A(bufoff, h, abase) do { _Pragma("unroll") for (int _i = 0; _i < 2; ++_i) { \
;         const char* _src = GATHER ? ((const char*)(abase) + gA[h][_i]) : ((const char*)(abase) + (size_t)(h) * hstep + voffA[_i]); \
;         __builtin_amdgcn_global_load_lds((const unsigned*)_src, (LAS unsigned*)(lds + (bufoff) + ldsw + _i * 8192), 16, 0, 0); } } while (0)
; #define PG8_LDA(dst, b, h) do { _Pragma("unroll") for (int m = 0; m < 4; ++m) PG8_LD2(dst[m], PG8_SA(b, h) + aoff + m * 2048); } while (0)
; #define PG8_WAIT_V(n) asm volatile("s_waitcnt vmcnt(" #n ")" ::: "memory")
; #define PG8_WAIT_L(n) asm volatile("s_waitcnt lgkmcnt(" #n ")" ::: "memory")
; #define PG8_BAR __builtin_amdgcn_s_barrier()
; #define PG8_SCHED __builtin_amdgcn_sched_barrier(0)
; template <int DT  , class Epi, class Sched, class Hook = NoHook>
; __device__ __forceinline__ void gemm_phase(LAS unsigned char* lds, const Sched& S, const Epi& E, int wave_s, LAS unsigned char* aux  ,
;                                            const Hook& H = Hook()  ) {
;     ...
;             PG8_LDA(At, 1, 1); PG8_STAGE(PG8_SB(1, 0), b3, voffB); PG8_STAGE(PG8_SB(1, 1), b3 + hstep, voffB); PG8_STAGE_A(PG8_SA(1, 0), 0, a3);
;             PG8_WAIT_V(8); PG8_WAIT_L(0); PG8_BAR; PG8_MMA(1, 0, At, B0); PG8_MMA(1, 1, At, B1); PG8_BAR; PG8_SCHED;
;         }
	s_mov_b32 m0, s35
	v_lshl_add_u64 v[200:201], v[200:201], 0, s[58:59]
	s_add_u32 s18, s18, 0x40080
	ds_read_b128 v[172:175], v192 offset:49152
	ds_read_b128 v[196:199], v192 offset:50176
	ds_read_b128 v[204:207], v192 offset:51200
	ds_read_b128 v[208:211], v192 offset:52224
	ds_read_b128 v[212:215], v192 offset:53248
	ds_read_b128 v[216:219], v192 offset:54272
	ds_read_b128 v[226:229], v192 offset:55296
	ds_read_b128 v[230:233], v192 offset:56320
	global_load_lds_dwordx4 v[200:201], off
	v_lshl_add_u64 v[200:201], v[234:235], 0, s[58:59]
	s_mov_b32 m0, s38
	s_addc_u32 s19, s19, 0
	global_load_lds_dwordx4 v[200:201], off
	v_lshl_add_u64 v[200:201], s[18:19], 0, v[32:33]
	s_mov_b32 m0, s44
	s_nop 0
	global_load_lds_dwordx4 v[200:201], off
	v_lshl_add_u64 v[200:201], s[18:19], 0, v[154:155]
	s_mov_b32 m0, s45
	s_nop 0
	global_load_lds_dwordx4 v[200:201], off
	v_lshl_add_u64 v[200:201], v[236:237], 0, s[58:59]
	s_mov_b32 m0, s40
	s_nop 0
	global_load_lds_dwordx4 v[200:201], off
	v_lshl_add_u64 v[200:201], v[238:239], 0, s[58:59]
	s_mov_b32 m0, s41
	s_nop 0
	global_load_lds_dwordx4 v[200:201], off
	s_waitcnt vmcnt(8)
	s_waitcnt lgkmcnt(0)
	s_barrier
	s_setprio 1
	s_waitcnt lgkmcnt(0)
	v_mfma_f32_16x16x32_bf16 v[54:57], v[138:141], v[172:175], v[54:57]
	v_mfma_f32_16x16x32_bf16 v[50:53], v[134:137], v[172:175], v[50:53]
	v_mfma_f32_16x16x32_bf16 v[38:41], v[138:141], v[204:207], v[38:41]
	v_mfma_f32_16x16x32_bf16 v[34:37], v[134:137], v[204:207], v[34:37]
	v_mfma_f32_16x16x32_bf16 v[20:23], v[138:141], v[212:215], v[20:23]
	v_mfma_f32_16x16x32_bf16 v[8:11], v[134:137], v[212:215], v[8:11]
	v_mfma_f32_16x16x32_bf16 v[4:7], v[138:141], v[226:229], v[4:7]
	v_mfma_f32_16x16x32_bf16 v[0:3], v[134:137], v[226:229], v[0:3]
	v_mfma_f32_16x16x32_bf16 v[54:57], v[130:133], v[196:199], v[54:57]
	v_mfma_f32_16x16x32_bf16 v[50:53], v[146:149], v[196:199], v[50:53]
	v_mfma_f32_16x16x32_bf16 v[38:41], v[130:133], v[208:211], v[38:41]
	v_mfma_f32_16x16x32_bf16 v[34:37], v[146:149], v[208:211], v[34:37]
	v_mfma_f32_16x16x32_bf16 v[20:23], v[130:133], v[216:219], v[20:23]
	v_mfma_f32_16x16x32_bf16 v[8:11], v[146:149], v[216:219], v[8:11]
	v_mfma_f32_16x16x32_bf16 v[4:7], v[130:133], v[230:233], v[4:7]
	v_mfma_f32_16x16x32_bf16 v[0:3], v[146:149], v[230:233], v[0:3]
	s_setprio 0
	s_setprio 1
	v_mfma_f32_16x16x32_bf16 v[58:61], v[142:145], v[172:175], v[58:61]
	v_mfma_f32_16x16x32_bf16 v[62:65], v[164:167], v[172:175], v[62:65]
	v_mfma_f32_16x16x32_bf16 v[42:45], v[142:145], v[204:207], v[42:45]
	v_mfma_f32_16x16x32_bf16 v[46:49], v[164:167], v[204:207], v[46:49]
	v_mfma_f32_16x16x32_bf16 v[24:27], v[142:145], v[212:215], v[24:27]
	v_mfma_f32_16x16x32_bf16 v[28:31], v[164:167], v[212:215], v[28:31]
	v_mfma_f32_16x16x32_bf16 v[12:15], v[142:145], v[226:229], v[12:15]
	v_mfma_f32_16x16x32_bf16 v[16:19], v[164:167], v[226:229], v[16:19]
	v_mfma_f32_16x16x32_bf16 v[58:61], v[150:153], v[196:199], v[58:61]
	v_mfma_f32_16x16x32_bf16 v[62:65], v[168:171], v[196:199], v[62:65]
	v_mfma_f32_16x16x32_bf16 v[42:45], v[150:153], v[208:211], v[42:45]
	v_mfma_f32_16x16x32_bf16 v[46:49], v[168:171], v[208:211], v[46:49]
	v_mfma_f32_16x16x32_bf16 v[24:27], v[150:153], v[216:219], v[24:27]
	v_mfma_f32_16x16x32_bf16 v[28:31], v[168:171], v[216:219], v[28:31]
	v_mfma_f32_16x16x32_bf16 v[12:15], v[150:153], v[230:233], v[12:15]
	v_mfma_f32_16x16x32_bf16 v[16:19], v[168:171], v[230:233], v[16:19]
	s_setprio 0
	s_barrier
	s_add_i32 s68, s68, 2
	s_add_u32 s16, s16, 0x100
	s_addc_u32 s17, s17, 0
	s_add_u32 s65, s65, 0x100
	s_addc_u32 s67, s67, 0
	s_cmp_gt_u32 s68, 13

; template <int DT  , class Epi, class Sched, class Hook = NoHook>
; __device__ __forceinline__ void gemm_phase(LAS unsigned char* lds, const Sched& S, const Epi& E, int wave_s, LAS unsigned char* aux  ,
;                                            const Hook& H = Hook()  ) {
;     ...
;         const bool has_next = S.next(ui + 1, nxt);
;         const char* nA = has_next ? S.aptr(nxt) : cA; const char* nB = has_next ? S.bptr(nxt) : cB;
;         {
;             if constexpr (GATHER) { if (has_next && wid == 0) __builtin_amdgcn_global_load_lds((const unsigned*)(S.list_src(nxt) + 4 * lane), (LAS unsigned*)(aux + ((ui + 1) & 1) * 1024), 16, 0, 0); }
;             if constexpr (Epi::PREFETCH) E.prefetch(cur, aux + 2048 + (ui & 1) * 3072, wid, lane);
;         }
;         for (int t = 0; t < nt; t += 2) {
;             const bool last = (t == nt - 2);
;             const char* a1 = cA + (size_t)(t + 1) * kstep;
;             const char* a2 = last ? nA : cA + (size_t)(t + 2) * kstep; const char* b2 = last ? nB : cB + (size_t)(t + 2) * kstep;
;             const char* a3 = a2 + kstep; const char* b3 = b2 + kstep;
;             PG8_LDB(B0, 0, 0); PG8_LDB(B1, 0, 1); PG8_SCHED; PG8_LDA(At, 0, 0); PG8_STAGE_A(PG8_SA(1, 1), 1, a1);
;             if (GATHER) { if (last && has_next) S.gather_lds(nxt, gA, tid, aux + ((ui + 1) & 1) * 1024); }
;             PG8_WAIT_V(8); PG8_WAIT_L(0); PG8_BAR; PG8_MMA(0, 0, At, B0); PG8_MMA(0, 1, At, B1); PG8_BAR; PG8_SCHED;
;             PG8_LDA(At, 0, 1); PG8_STAGE(PG8_SB(0, 0), b2, voffB); PG8_STAGE(PG8_SB(0, 1), b2 + hstep, voffB); PG8_STAGE_A(PG8_SA(0, 0), 0, a2);
;             PG8_WAIT_V(8); PG8_WAIT_L(0); PG8_BAR; PG8_MMA(1, 0, At, B0); PG8_MMA(1, 1, At, B1); PG8_BAR; PG8_SCHED;
;             PG8_LDB(B0, 1, 0); PG8_LDB(B1, 1, 1); PG8_SCHED; PG8_LDA(At, 1, 0); PG8_STAGE_A(PG8_SA(0, 1), 1, a2);
;             PG8_WAIT_V(8); PG8_WAIT_L(0); PG8_BAR; PG8_MMA(0, 0, At, B0); PG8_MMA(0, 1, At, B1); PG8_BAR; PG8_SCHED;
;             PG8_LDA(At, 1, 1); PG8_STAGE(PG8_SB(1, 0), b3, voffB); PG8_STAGE(PG8_SB(1, 1), b3 + hstep, voffB); PG8_STAGE_A(PG8_SA(1, 0), 0, a3);
;             PG8_WAIT_V(8); PG8_WAIT_L(0); PG8_BAR; PG8_MMA(1, 0, At, B0); PG8_MMA(1, 1, At, B1); PG8_BAR; PG8_SCHED;
;         }
;         if (wr == 0) PG8_BAR;
;         E(acc, cur, wr, wc, fr, fq, aux + 2048 + (ui & 1) * 3072);
;         H(ui);
;         if (!has_next) break;
.LBB0_576:
	s_lshl_b32 s4, s74, 10
	s_and_b32 s4, s4, 0x400
	v_lshlrev_b32_e32 v0, 2, v208
	s_add_i32 s77, s4, 0
	v_add_u32_e32 v0, 0, v0
	v_readlane_b32 s24, v253, 36
	s_add_i32 s77, s77, 0x20240
	v_add_u32_e32 v209, 0x20040, v0
	v_lshl_add_u64 v[214:215], v[2:3], 0, s[54:55]
	s_mov_b32 s89, -2
	v_readlane_b32 s25, v253, 37
	ds_read_b128 v[130:133], v230
	ds_read_b128 v[134:137], v231
	ds_read_b128 v[154:157], v226
	ds_read_b128 v[42:45], v227
	ds_read_b128 v[158:161], v232
	ds_read_b128 v[50:53], v233
	ds_read_b128 v[122:125], v234
	ds_read_b128 v[126:129], v235
	s_cmp_eq_u32 s89, 4
	s_cselect_b64 s[4:5], -1, 0
	s_add_i32 m0, s28, 0xc000
	ds_read_b128 v[186:189], v242
	ds_read_b128 v[190:193], v242 offset:1024
	ds_read_b128 v[178:181], v242 offset:2048
	ds_read_b128 v[182:185], v242 offset:3072
	ds_read_b128 v[170:173], v242 offset:4096
	ds_read_b128 v[174:177], v242 offset:5120
	ds_read_b128 v[162:165], v242 offset:6144
	ds_read_b128 v[166:169], v242 offset:7168
	global_load_lds_dwordx4 v206, s[24:25]
	s_add_i32 m0, s28, 0xe000
	s_and_b64 s[18:19], s[22:23], s[4:5]
	global_load_lds_dwordx4 v204, s[24:25]
	s_andn2_b64 vcc, exec, s[18:19]
	v_mov_b32_e32 v207, v33
	v_mov_b32_e32 v205, v33
	v_mov_b64_e32 v[216:217], v[206:207]
	s_waitcnt vmcnt(8)
	s_add_u32 s42, s24, 0x80
	s_waitcnt lgkmcnt(0)
	s_addc_u32 s43, s25, 0
	s_and_b64 s[18:19], s[4:5], exec
	s_cselect_b32 s19, s37, s43
	s_cselect_b32 s18, s36, s42
	v_cndmask_b32_e64 v219, v215, v211, s[4:5]
	v_cndmask_b32_e64 v218, v214, v210, s[4:5]
	s_barrier
	s_setprio 1
	s_waitcnt lgkmcnt(0)
	v_mfma_i32_16x16x64_i8 v[150:153], v[154:157], v[186:189], 0
	v_mfma_i32_16x16x64_i8 v[146:149], v[134:137], v[186:189], 0
	v_mfma_i32_16x16x64_i8 v[142:145], v[154:157], v[178:181], 0
	v_mfma_i32_16x16x64_i8 v[138:141], v[134:137], v[178:181], 0
	v_mfma_i32_16x16x64_i8 v[118:121], v[154:157], v[170:173], 0
	v_mfma_i32_16x16x64_i8 v[114:117], v[134:137], v[170:173], 0
	v_mfma_i32_16x16x64_i8 v[110:113], v[154:157], v[162:165], 0
	v_mfma_i32_16x16x64_i8 v[106:109], v[134:137], v[162:165], 0
	v_mfma_i32_16x16x64_i8 v[150:153], v[130:133], v[190:193], v[150:153]
	v_mfma_i32_16x16x64_i8 v[146:149], v[158:161], v[190:193], v[146:149]
	v_mfma_i32_16x16x64_i8 v[142:145], v[130:133], v[182:185], v[142:145]
	v_mfma_i32_16x16x64_i8 v[138:141], v[158:161], v[182:185], v[138:141]
	v_mfma_i32_16x16x64_i8 v[118:121], v[130:133], v[174:177], v[118:121]
	v_mfma_i32_16x16x64_i8 v[114:117], v[158:161], v[174:177], v[114:117]
	v_mfma_i32_16x16x64_i8 v[110:113], v[130:133], v[166:169], v[110:113]
	v_mfma_i32_16x16x64_i8 v[106:109], v[158:161], v[166:169], v[106:109]
	s_setprio 0
	s_setprio 1
	v_mfma_i32_16x16x64_i8 v[66:69], v[42:45], v[186:189], 0
	v_mfma_i32_16x16x64_i8 v[70:73], v[122:125], v[186:189], 0
	v_mfma_i32_16x16x64_i8 v[58:61], v[42:45], v[178:181], 0
	v_mfma_i32_16x16x64_i8 v[62:65], v[122:125], v[178:181], 0
	v_mfma_i32_16x16x64_i8 v[46:49], v[42:45], v[170:173], 0
	v_mfma_i32_16x16x64_i8 v[54:57], v[122:125], v[170:173], 0
	v_mfma_i32_16x16x64_i8 v[34:37], v[42:45], v[162:165], 0
	v_mfma_i32_16x16x64_i8 v[38:41], v[122:125], v[162:165], 0
	v_mfma_i32_16x16x64_i8 v[66:69], v[50:53], v[190:193], v[66:69]
	v_mfma_i32_16x16x64_i8 v[70:73], v[126:129], v[190:193], v[70:73]
	v_mfma_i32_16x16x64_i8 v[58:61], v[50:53], v[182:185], v[58:61]
	v_mfma_i32_16x16x64_i8 v[62:65], v[126:129], v[182:185], v[62:65]
	v_mfma_i32_16x16x64_i8 v[46:49], v[50:53], v[174:177], v[46:49]
	v_mfma_i32_16x16x64_i8 v[54:57], v[126:129], v[174:177], v[54:57]
	v_mfma_i32_16x16x64_i8 v[34:37], v[50:53], v[166:169], v[34:37]
	v_mfma_i32_16x16x64_i8 v[38:41], v[126:129], v[166:169], v[38:41]
	s_setprio 0
	s_barrier
	s_mov_b32 m0, s29
	v_lshl_add_u64 v[244:245], v[218:219], 0, v[198:199]
	ds_read_b128 v[162:165], v242 offset:16384
	ds_read_b128 v[166:169], v242 offset:17408
	ds_read_b128 v[170:173], v242 offset:18432
	ds_read_b128 v[174:177], v242 offset:19456
	ds_read_b128 v[178:181], v242 offset:20480
	ds_read_b128 v[182:185], v242 offset:21504
	ds_read_b128 v[186:189], v242 offset:22528
	ds_read_b128 v[190:193], v242 offset:23552
	global_load_lds_dwordx4 v[244:245], off
	v_lshl_add_u64 v[246:247], v[218:219], 0, v[196:197]
	s_mov_b32 m0, s30
	v_lshl_add_u64 v[248:249], v[218:219], 0, s[70:71]
	global_load_lds_dwordx4 v[246:247], off
	v_lshl_add_u64 v[194:195], v[248:249], 0, v[198:199]
	s_mov_b32 m0, s31
	v_mov_b32_e32 v201, v33
	global_load_lds_dwordx4 v[194:195], off
	v_lshl_add_u64 v[194:195], v[248:249], 0, v[196:197]
	s_mov_b32 m0, s34
	v_lshl_add_u64 v[248:249], s[18:19], 0, v[200:201]
	global_load_lds_dwordx4 v[194:195], off
	s_mov_b32 m0, s28
	v_lshl_add_u64 v[194:195], s[18:19], 0, v[32:33]
	global_load_lds_dwordx4 v32, s[18:19]
	s_mov_b32 m0, s35
	s_nop 0
	global_load_lds_dwordx4 v200, s[18:19]
	s_waitcnt vmcnt(8)
	s_waitcnt lgkmcnt(0)
	s_barrier
; #define PG8_STAGE_A(bufoff, h, abase) do { _Pragma("unroll") for (int _i = 0; _i < 2; ++_i) { \
;         const char* _src = GATHER ? ((const char*)(abase) + gA[h][_i]) : ((const char*)(abase) + (size_t)(h) * hstep + voffA[_i]); \
;         __builtin_amdgcn_global_load_lds((const unsigned*)_src, (LAS unsigned*)(lds + (bufoff) + ldsw + _i * 8192), 16, 0, 0); } } while (0)
; #define PG8_LDA(dst, b, h) do { _Pragma("unroll") for (int m = 0; m < 4; ++m) PG8_LD2(dst[m], PG8_SA(b, h) + aoff + m * 2048); } while (0)
; #define PG8_LDB(dst, b, h) do { _Pragma("unroll") for (int n = 0; n < 2; ++n) PG8_LD2(dst[n], PG8_SB(b, h) + boff + n * 2048); } while (0)
; #define PG8_WAIT_V(n) asm volatile("s_waitcnt vmcnt(" #n ")" ::: "memory")
; #define PG8_WAIT_L(n) asm volatile("s_waitcnt lgkmcnt(" #n ")" ::: "memory")
; #define PG8_BAR __builtin_amdgcn_s_barrier()
; #define PG8_SCHED __builtin_amdgcn_sched_barrier(0)
; template <int DT  , class Epi, class Sched, class Hook = NoHook>
; __device__ __forceinline__ void gemm_phase(LAS unsigned char* lds, const Sched& S, const Epi& E, int wave_s, LAS unsigned char* aux  ,
;                                            const Hook& H = Hook()  ) {
;     ...
;             PG8_WAIT_V(8); PG8_WAIT_L(0); PG8_BAR; PG8_MMA(1, 0, At, B0); PG8_MMA(1, 1, At, B1); PG8_BAR; PG8_SCHED;
;             PG8_LDB(B0, 1, 0); PG8_LDB(B1, 1, 1); PG8_SCHED; PG8_LDA(At, 1, 0); PG8_STAGE_A(PG8_SA(0, 1), 1, a2);
;             PG8_WAIT_V(8); PG8_WAIT_L(0); PG8_BAR; PG8_MMA(0, 0, At, B0); PG8_MMA(0, 1, At, B1); PG8_BAR; PG8_SCHED;
	s_setprio 1
	s_waitcnt lgkmcnt(0)
	v_mfma_i32_16x16x64_i8 v[102:105], v[154:157], v[162:165], 0
	v_mfma_i32_16x16x64_i8 v[98:101], v[134:137], v[162:165], 0
	v_mfma_i32_16x16x64_i8 v[94:97], v[154:157], v[170:173], 0
	v_mfma_i32_16x16x64_i8 v[90:93], v[134:137], v[170:173], 0
	v_mfma_i32_16x16x64_i8 v[86:89], v[154:157], v[178:181], 0
	v_mfma_i32_16x16x64_i8 v[82:85], v[134:137], v[178:181], 0
	v_mfma_i32_16x16x64_i8 v[78:81], v[154:157], v[186:189], 0
	v_mfma_i32_16x16x64_i8 v[74:77], v[134:137], v[186:189], 0
	v_mfma_i32_16x16x64_i8 v[102:105], v[130:133], v[166:169], v[102:105]
	v_mfma_i32_16x16x64_i8 v[98:101], v[158:161], v[166:169], v[98:101]
	v_mfma_i32_16x16x64_i8 v[94:97], v[130:133], v[174:177], v[94:97]
	v_mfma_i32_16x16x64_i8 v[90:93], v[158:161], v[174:177], v[90:93]
	v_mfma_i32_16x16x64_i8 v[86:89], v[130:133], v[182:185], v[86:89]
	v_mfma_i32_16x16x64_i8 v[82:85], v[158:161], v[182:185], v[82:85]
	v_mfma_i32_16x16x64_i8 v[78:81], v[130:133], v[190:193], v[78:81]
	v_mfma_i32_16x16x64_i8 v[74:77], v[158:161], v[190:193], v[74:77]
	s_setprio 0
	s_setprio 1
	v_mfma_i32_16x16x64_i8 v[24:27], v[42:45], v[162:165], 0
	v_mfma_i32_16x16x64_i8 v[28:31], v[122:125], v[162:165], 0
	v_mfma_i32_16x16x64_i8 v[16:19], v[42:45], v[170:173], 0
	v_mfma_i32_16x16x64_i8 v[20:23], v[122:125], v[170:173], 0
	v_mfma_i32_16x16x64_i8 v[8:11], v[42:45], v[178:181], 0
	v_mfma_i32_16x16x64_i8 v[12:15], v[122:125], v[178:181], 0
	v_mfma_i32_16x16x64_i8 v[0:3], v[42:45], v[186:189], 0
	v_mfma_i32_16x16x64_i8 v[4:7], v[122:125], v[186:189], 0
	v_mfma_i32_16x16x64_i8 v[24:27], v[50:53], v[166:169], v[24:27]
	v_mfma_i32_16x16x64_i8 v[28:31], v[126:129], v[166:169], v[28:31]
	v_mfma_i32_16x16x64_i8 v[16:19], v[50:53], v[174:177], v[16:19]
	v_mfma_i32_16x16x64_i8 v[20:23], v[126:129], v[174:177], v[20:23]
	v_mfma_i32_16x16x64_i8 v[8:11], v[50:53], v[182:185], v[8:11]
	v_mfma_i32_16x16x64_i8 v[12:15], v[126:129], v[182:185], v[12:15]
	v_mfma_i32_16x16x64_i8 v[0:3], v[50:53], v[190:193], v[0:3]
	v_mfma_i32_16x16x64_i8 v[4:7], v[126:129], v[190:193], v[4:7]
	s_setprio 0
	s_barrier
	ds_read_b128 v[42:45], v236
	ds_read_b128 v[50:53], v237
	ds_read_b128 v[122:125], v228
	ds_read_b128 v[126:129], v229
	ds_read_b128 v[130:133], v238
	ds_read_b128 v[134:137], v239
	ds_read_b128 v[154:157], v240
	ds_read_b128 v[158:161], v241
	s_mov_b32 m0, s38
	v_lshl_add_u64 v[216:217], s[18:19], 0, v[216:217]
	ds_read_b128 v[162:165], v242 offset:32768
	ds_read_b128 v[166:169], v242 offset:33792
	ds_read_b128 v[170:173], v242 offset:34816
	ds_read_b128 v[174:177], v242 offset:35840
	ds_read_b128 v[178:181], v242 offset:36864
	ds_read_b128 v[182:185], v242 offset:37888
	ds_read_b128 v[186:189], v242 offset:38912
	ds_read_b128 v[190:193], v242 offset:39936
	global_load_lds_dwordx4 v[216:217], off
	v_lshl_add_u64 v[216:217], s[18:19], 0, v[204:205]
	s_mov_b32 m0, s44
	s_nop 0
	global_load_lds_dwordx4 v[216:217], off
	s_waitcnt vmcnt(8)
	s_waitcnt lgkmcnt(0)
	s_barrier
	s_setprio 1
	s_waitcnt lgkmcnt(0)
	v_mfma_i32_16x16x64_i8 v[150:153], v[122:125], v[162:165], v[150:153]
	v_mfma_i32_16x16x64_i8 v[146:149], v[50:53], v[162:165], v[146:149]
	v_mfma_i32_16x16x64_i8 v[142:145], v[122:125], v[170:173], v[142:145]
	v_mfma_i32_16x16x64_i8 v[138:141], v[50:53], v[170:173], v[138:141]
	v_mfma_i32_16x16x64_i8 v[118:121], v[122:125], v[178:181], v[118:121]
	v_mfma_i32_16x16x64_i8 v[114:117], v[50:53], v[178:181], v[114:117]
	v_mfma_i32_16x16x64_i8 v[110:113], v[122:125], v[186:189], v[110:113]
	v_mfma_i32_16x16x64_i8 v[106:109], v[50:53], v[186:189], v[106:109]
	v_mfma_i32_16x16x64_i8 v[150:153], v[42:45], v[166:169], v[150:153]
	v_mfma_i32_16x16x64_i8 v[146:149], v[130:133], v[166:169], v[146:149]
	v_mfma_i32_16x16x64_i8 v[142:145], v[42:45], v[174:177], v[142:145]
	v_mfma_i32_16x16x64_i8 v[138:141], v[130:133], v[174:177], v[138:141]
	v_mfma_i32_16x16x64_i8 v[118:121], v[42:45], v[182:185], v[118:121]
	v_mfma_i32_16x16x64_i8 v[114:117], v[130:133], v[182:185], v[114:117]
	v_mfma_i32_16x16x64_i8 v[110:113], v[42:45], v[190:193], v[110:113]
	v_mfma_i32_16x16x64_i8 v[106:109], v[130:133], v[190:193], v[106:109]
	s_setprio 0
	s_setprio 1
	v_mfma_i32_16x16x64_i8 v[66:69], v[126:129], v[162:165], v[66:69]
	v_mfma_i32_16x16x64_i8 v[70:73], v[154:157], v[162:165], v[70:73]
	v_mfma_i32_16x16x64_i8 v[58:61], v[126:129], v[170:173], v[58:61]
	v_mfma_i32_16x16x64_i8 v[62:65], v[154:157], v[170:173], v[62:65]
	v_mfma_i32_16x16x64_i8 v[46:49], v[126:129], v[178:181], v[46:49]
	v_mfma_i32_16x16x64_i8 v[54:57], v[154:157], v[178:181], v[54:57]
	v_mfma_i32_16x16x64_i8 v[34:37], v[126:129], v[186:189], v[34:37]
	v_mfma_i32_16x16x64_i8 v[38:41], v[154:157], v[186:189], v[38:41]
	v_mfma_i32_16x16x64_i8 v[66:69], v[134:137], v[166:169], v[66:69]
	v_mfma_i32_16x16x64_i8 v[70:73], v[158:161], v[166:169], v[70:73]
	v_mfma_i32_16x16x64_i8 v[58:61], v[134:137], v[174:177], v[58:61]
	v_mfma_i32_16x16x64_i8 v[62:65], v[158:161], v[174:177], v[62:65]
	v_mfma_i32_16x16x64_i8 v[46:49], v[134:137], v[182:185], v[46:49]
	v_mfma_i32_16x16x64_i8 v[54:57], v[158:161], v[182:185], v[54:57]
	v_mfma_i32_16x16x64_i8 v[34:37], v[134:137], v[190:193], v[34:37]
	v_mfma_i32_16x16x64_i8 v[38:41], v[158:161], v[190:193], v[38:41]
	s_setprio 0
	s_barrier
; #define PG8_STAGE(bufoff, gbase, voff) do { _Pragma("unroll") for (int _i = 0; _i < 2; ++_i) \
;         __builtin_amdgcn_global_load_lds((const unsigned*)((const char*)(gbase) + (voff)[_i]), (LAS unsigned*)(lds + (bufoff) + ldsw + _i * 8192), 16, 0, 0); } while (0)
; #define PG8_STAGE_A(bufoff, h, abase) do { _Pragma("unroll") for (int _i = 0; _i < 2; ++_i) { \
;         const char* _src = GATHER ? ((const char*)(abase) + gA[h][_i]) : ((const char*)(abase) + (size_t)(h) * hstep + voffA[_i]); \
;         __builtin_amdgcn_global_load_lds((const unsigned*)_src, (LAS unsigned*)(lds + (bufoff) + ldsw + _i * 8192), 16, 0, 0); } } while (0)
; #define PG8_LDA(dst, b, h) do { _Pragma("unroll") for (int m = 0; m < 4; ++m) PG8_LD2(dst[m], PG8_SA(b, h) + aoff + m * 2048); } while (0)
; #define PG8_WAIT_V(n) asm volatile("s_waitcnt vmcnt(" #n ")" ::: "memory")
; #define PG8_WAIT_L(n) asm volatile("s_waitcnt lgkmcnt(" #n ")" ::: "memory")
; #define PG8_BAR __builtin_amdgcn_s_barrier()
; #define PG8_SCHED __builtin_amdgcn_sched_barrier(0)
; template <int DT  , class Epi, class Sched, class Hook = NoHook>
; __device__ __forceinline__ void gemm_phase(LAS unsigned char* lds, const Sched& S, const Epi& E, int wave_s, LAS unsigned char* aux  ,
;                                            const Hook& H = Hook()  ) {
;     ...
;             PG8_LDA(At, 1, 1); PG8_STAGE(PG8_SB(1, 0), b3, voffB); PG8_STAGE(PG8_SB(1, 1), b3 + hstep, voffB); PG8_STAGE_A(PG8_SA(1, 0), 0, a3);
;             PG8_WAIT_V(8); PG8_WAIT_L(0); PG8_BAR; PG8_MMA(1, 0, At, B0); PG8_MMA(1, 1, At, B1); PG8_BAR; PG8_SCHED;
;         }
	s_mov_b32 m0, s45
	v_lshl_add_u64 v[216:217], v[244:245], 0, s[58:59]
	ds_read_b128 v[162:165], v242 offset:49152
	ds_read_b128 v[166:169], v242 offset:50176
	ds_read_b128 v[170:173], v242 offset:51200
	ds_read_b128 v[174:177], v242 offset:52224
	ds_read_b128 v[178:181], v242 offset:53248
	ds_read_b128 v[182:185], v242 offset:54272
	ds_read_b128 v[186:189], v242 offset:55296
	ds_read_b128 v[190:193], v242 offset:56320
	global_load_lds_dwordx4 v[216:217], off
	v_lshl_add_u64 v[216:217], v[246:247], 0, s[58:59]
	s_mov_b32 m0, s46
	v_lshl_add_u64 v[194:195], v[194:195], 0, s[58:59]
	global_load_lds_dwordx4 v[216:217], off
	v_lshl_add_u64 v[216:217], v[218:219], 0, s[62:63]
	v_lshl_add_u64 v[218:219], v[216:217], 0, v[198:199]
	s_mov_b32 m0, s51
	v_lshl_add_u64 v[216:217], v[216:217], 0, v[196:197]
	global_load_lds_dwordx4 v[218:219], off
	s_mov_b32 m0, s57
	s_nop 0
	global_load_lds_dwordx4 v[216:217], off
	s_mov_b32 m0, s47
	s_nop 0
	global_load_lds_dwordx4 v[194:195], off
	v_lshl_add_u64 v[194:195], v[248:249], 0, s[58:59]
	s_mov_b32 m0, s48
	s_nop 0
	global_load_lds_dwordx4 v[194:195], off
	s_waitcnt vmcnt(8)
	s_waitcnt lgkmcnt(0)
	s_barrier
	s_setprio 1
	s_waitcnt lgkmcnt(0)
	v_mfma_i32_16x16x64_i8 v[102:105], v[122:125], v[162:165], v[102:105]
	v_mfma_i32_16x16x64_i8 v[94:97], v[122:125], v[170:173], v[94:97]
	v_mfma_i32_16x16x64_i8 v[86:89], v[122:125], v[178:181], v[86:89]
	v_mfma_i32_16x16x64_i8 v[78:81], v[122:125], v[186:189], v[78:81]
	v_mfma_i32_16x16x64_i8 v[102:105], v[42:45], v[166:169], v[102:105]
	v_mfma_i32_16x16x64_i8 v[98:101], v[50:53], v[162:165], v[98:101]
	v_mfma_i32_16x16x64_i8 v[94:97], v[42:45], v[174:177], v[94:97]
	v_mfma_i32_16x16x64_i8 v[90:93], v[50:53], v[170:173], v[90:93]
	v_mfma_i32_16x16x64_i8 v[86:89], v[42:45], v[182:185], v[86:89]
	v_mfma_i32_16x16x64_i8 v[82:85], v[50:53], v[178:181], v[82:85]
	v_mfma_i32_16x16x64_i8 v[78:81], v[42:45], v[190:193], v[78:81]
	v_mfma_i32_16x16x64_i8 v[42:45], v[50:53], v[186:189], v[74:77]
	v_mfma_i32_16x16x64_i8 v[98:101], v[130:133], v[166:169], v[98:101]
	v_mfma_i32_16x16x64_i8 v[90:93], v[130:133], v[174:177], v[90:93]
	v_mfma_i32_16x16x64_i8 v[82:85], v[130:133], v[182:185], v[82:85]
	v_mfma_i32_16x16x64_i8 v[74:77], v[130:133], v[190:193], v[42:45]
	s_setprio 0
	s_setprio 1
	v_mfma_i32_16x16x64_i8 v[24:27], v[126:129], v[162:165], v[24:27]
	v_mfma_i32_16x16x64_i8 v[28:31], v[154:157], v[162:165], v[28:31]
	v_mfma_i32_16x16x64_i8 v[16:19], v[126:129], v[170:173], v[16:19]
	v_mfma_i32_16x16x64_i8 v[20:23], v[154:157], v[170:173], v[20:23]
	v_mfma_i32_16x16x64_i8 v[8:11], v[126:129], v[178:181], v[8:11]
	v_mfma_i32_16x16x64_i8 v[12:15], v[154:157], v[178:181], v[12:15]
	v_mfma_i32_16x16x64_i8 v[0:3], v[126:129], v[186:189], v[0:3]
	v_mfma_i32_16x16x64_i8 v[4:7], v[154:157], v[186:189], v[4:7]
	v_mfma_i32_16x16x64_i8 v[24:27], v[134:137], v[166:169], v[24:27]
	v_mfma_i32_16x16x64_i8 v[28:31], v[158:161], v[166:169], v[28:31]
	v_mfma_i32_16x16x64_i8 v[16:19], v[134:137], v[174:177], v[16:19]
	v_mfma_i32_16x16x64_i8 v[20:23], v[158:161], v[174:177], v[20:23]
	v_mfma_i32_16x16x64_i8 v[8:11], v[134:137], v[182:185], v[8:11]
	v_mfma_i32_16x16x64_i8 v[12:15], v[158:161], v[182:185], v[12:15]
	v_mfma_i32_16x16x64_i8 v[0:3], v[134:137], v[190:193], v[0:3]
	v_mfma_i32_16x16x64_i8 v[4:7], v[158:161], v[190:193], v[4:7]
	s_setprio 0
	s_barrier
	s_add_i32 s89, s89, 2
	s_add_u32 s24, s24, 0x100
	s_addc_u32 s25, s25, 0
	s_cmp_gt_u32 s89, 5
	v_lshl_add_u64 v[214:215], v[214:215], 0, s[54:55]
	s_branch .LBB0_579

; #define PG8_LDA(dst, b, h) do { _Pragma("unroll") for (int m = 0; m < 4; ++m) PG8_LD2(dst[m], PG8_SA(b, h) + aoff + m * 2048); } while (0)
; #define PG8_BAR __builtin_amdgcn_s_barrier()
; template <int DT  , class Epi, class Sched, class Hook = NoHook>
; __device__ __forceinline__ void gemm_phase(LAS unsigned char* lds, const Sched& S, const Epi& E, int wave_s, LAS unsigned char* aux  ,
;                                            const Hook& H = Hook()  ) {
;     ...
;         for (int t = 0; t < nt; t += 2) {
;             const bool last = (t == nt - 2);
;             const char* a1 = cA + (size_t)(t + 1) * kstep;
;             const char* a2 = last ? nA : cA + (size_t)(t + 2) * kstep; const char* b2 = last ? nB : cB + (size_t)(t + 2) * kstep;
;             const char* a3 = a2 + kstep; const char* b3 = b2 + kstep;
;             PG8_LDB(B0, 0, 0); PG8_LDB(B1, 0, 1); PG8_SCHED; PG8_LDA(At, 0, 0); PG8_STAGE_A(PG8_SA(1, 1), 1, a1);
;             if (GATHER) { if (last && has_next) S.gather_lds(nxt, gA, tid, aux + ((ui + 1) & 1) * 1024); }
;             PG8_WAIT_V(8); PG8_WAIT_L(0); PG8_BAR; PG8_MMA(0, 0, At, B0); PG8_MMA(0, 1, At, B1); PG8_BAR; PG8_SCHED;
;             PG8_LDA(At, 0, 1); PG8_STAGE(PG8_SB(0, 0), b2, voffB); PG8_STAGE(PG8_SB(0, 1), b2 + hstep, voffB); PG8_STAGE_A(PG8_SA(0, 0), 0, a2);
;             PG8_WAIT_V(8); PG8_WAIT_L(0); PG8_BAR; PG8_MMA(1, 0, At, B0); PG8_MMA(1, 1, At, B1); PG8_BAR; PG8_SCHED;
;             PG8_LDB(B0, 1, 0); PG8_LDB(B1, 1, 1); PG8_SCHED; PG8_LDA(At, 1, 0); PG8_STAGE_A(PG8_SA(0, 1), 1, a2);
;             PG8_WAIT_V(8); PG8_WAIT_L(0); PG8_BAR; PG8_MMA(0, 0, At, B0); PG8_MMA(0, 1, At, B1); PG8_BAR; PG8_SCHED;
;             PG8_LDA(At, 1, 1); PG8_STAGE(PG8_SB(1, 0), b3, voffB); PG8_STAGE(PG8_SB(1, 1), b3 + hstep, voffB); PG8_STAGE_A(PG8_SA(1, 0), 0, a3);
;             PG8_WAIT_V(8); PG8_WAIT_L(0); PG8_BAR; PG8_MMA(1, 0, At, B0); PG8_MMA(1, 1, At, B1); PG8_BAR; PG8_SCHED;
;         }
;         if (wr == 0) PG8_BAR;
;         E(acc, cur, wr, wc, fr, fq, aux + 2048 + (ui & 1) * 3072);
;         H(ui);
;         if (!has_next) break;
; #pragma unroll
;         for (int a = 0; a < 2; ++a)
; #pragma unroll
;             for (int b = 0; b < 2; ++b)
; #pragma unroll
;                 for (int m = 0; m < 4; ++m)
; #pragma unroll
;                     for (int n = 0; n < 2; ++n) acc[a][b][m][n] = (acc_t){0, 0, 0, 0};
.LBB0_650:
	s_ashr_i32 s15, s14, 31
	s_lshl_b64 s[18:19], s[14:15], 18
	v_readlane_b32 s20, v253, 44
	v_readlane_b32 s21, v253, 45
	s_add_u32 s20, s20, s18
	s_addc_u32 s21, s21, s19
	s_and_b64 s[18:19], s[24:25], exec
	s_cselect_b32 s15, s21, s23
	s_cselect_b32 s24, s20, s22
	s_add_u32 s22, s22, 0x20080
	s_addc_u32 s23, s23, 0
	v_lshl_add_u64 v[180:181], v[0:1], 0, s[54:55]
	s_mov_b32 s25, -2
	ds_read_b128 v[28:31], v197
	ds_read_b128 v[16:19], v198
	ds_read_b128 v[24:27], v171
	ds_read_b128 v[0:3], v192
	ds_read_b128 v[20:23], v199
	ds_read_b128 v[4:7], v200
	ds_read_b128 v[8:11], v201
	ds_read_b128 v[12:15], v202
	s_add_u32 s18, s22, 0xfffe0080
	s_addc_u32 s19, s23, -1
	s_cmp_eq_u32 s25, 4
	s_cselect_b64 vcc, -1, 0
	s_cselect_b32 s19, s15, s19
	s_cselect_b32 s18, s24, s18
	v_cndmask_b32_e32 v183, v181, v179, vcc
	v_cndmask_b32_e32 v182, v180, v178, vcc
	v_lshl_add_u64 v[194:195], s[22:23], 0, v[172:173]
	s_add_i32 m0, s28, 0xc000
	ds_read_b128 v[184:187], v210
	ds_read_b128 v[188:191], v210 offset:1024
	ds_read_b128 v[226:229], v210 offset:2048
	ds_read_b128 v[230:233], v210 offset:3072
	ds_read_b128 v[234:237], v210 offset:4096
	ds_read_b128 v[238:241], v210 offset:5120
	ds_read_b128 v[242:245], v210 offset:6144
	ds_read_b128 v[246:249], v210 offset:7168
	global_load_lds_dwordx4 v[194:195], off
	v_lshl_add_u64 v[194:195], s[22:23], 0, v[174:175]
	s_add_i32 m0, s28, 0xe000
	s_nop 0
	global_load_lds_dwordx4 v[194:195], off
	s_waitcnt vmcnt(8)
	s_waitcnt lgkmcnt(0)
	s_barrier
	s_setprio 1
	s_waitcnt lgkmcnt(0)
	v_mfma_scale_f32_16x16x128_f8f6f4 v[154:157], v[24:31], v[184:191], 0, v220, v220 op_sel_hi:[0,0,0]
	v_mfma_scale_f32_16x16x128_f8f6f4 v[158:161], v[16:23], v[184:191], 0, v220, v220 op_sel_hi:[0,0,0]
	v_mfma_scale_f32_16x16x128_f8f6f4 v[138:141], v[24:31], v[226:233], 0, v220, v220 op_sel_hi:[0,0,0]
	v_mfma_scale_f32_16x16x128_f8f6f4 v[142:145], v[16:23], v[226:233], 0, v220, v220 op_sel_hi:[0,0,0]
	v_mfma_scale_f32_16x16x128_f8f6f4 v[122:125], v[24:31], v[234:241], 0, v220, v220 op_sel_hi:[0,0,0]
	v_mfma_scale_f32_16x16x128_f8f6f4 v[126:129], v[16:23], v[234:241], 0, v220, v220 op_sel_hi:[0,0,0]
	v_mfma_scale_f32_16x16x128_f8f6f4 v[106:109], v[24:31], v[242:249], 0, v220, v220 op_sel_hi:[0,0,0]
	v_mfma_scale_f32_16x16x128_f8f6f4 v[110:113], v[16:23], v[242:249], 0, v220, v220 op_sel_hi:[0,0,0]
	s_setprio 0
	s_setprio 1
	v_mfma_scale_f32_16x16x128_f8f6f4 v[146:149], v[0:7], v[184:191], 0, v220, v220 op_sel_hi:[0,0,0]
	v_mfma_scale_f32_16x16x128_f8f6f4 v[150:153], v[8:15], v[184:191], 0, v220, v220 op_sel_hi:[0,0,0]
	v_mfma_scale_f32_16x16x128_f8f6f4 v[130:133], v[0:7], v[226:233], 0, v220, v220 op_sel_hi:[0,0,0]
	v_mfma_scale_f32_16x16x128_f8f6f4 v[134:137], v[8:15], v[226:233], 0, v220, v220 op_sel_hi:[0,0,0]
	v_mfma_scale_f32_16x16x128_f8f6f4 v[114:117], v[0:7], v[234:241], 0, v220, v220 op_sel_hi:[0,0,0]
	v_mfma_scale_f32_16x16x128_f8f6f4 v[118:121], v[8:15], v[234:241], 0, v220, v220 op_sel_hi:[0,0,0]
	v_mfma_scale_f32_16x16x128_f8f6f4 v[98:101], v[0:7], v[242:249], 0, v220, v220 op_sel_hi:[0,0,0]
	v_mfma_scale_f32_16x16x128_f8f6f4 v[102:105], v[8:15], v[242:249], 0, v220, v220 op_sel_hi:[0,0,0]
	s_setprio 0
	s_barrier
	s_mov_b32 m0, s29
	v_lshl_add_u64 v[184:185], v[182:183], 0, v[166:167]
	ds_read_b128 v[226:229], v210 offset:16384
	ds_read_b128 v[230:233], v210 offset:17408
	ds_read_b128 v[234:237], v210 offset:18432
	ds_read_b128 v[238:241], v210 offset:19456
	ds_read_b128 v[242:245], v210 offset:20480
	ds_read_b128 v[246:249], v210 offset:21504
	ds_read_b128 v[212:215], v210 offset:22528
	ds_read_b128 v[216:219], v210 offset:23552
	global_load_lds_dwordx4 v[184:185], off
	v_lshl_add_u64 v[186:187], v[182:183], 0, v[162:163]
	s_mov_b32 m0, s30
	v_lshl_add_u64 v[188:189], v[182:183], 0, s[70:71]
	global_load_lds_dwordx4 v[186:187], off
	v_lshl_add_u64 v[190:191], v[188:189], 0, v[166:167]
	s_mov_b32 m0, s31
	v_lshl_add_u64 v[188:189], v[188:189], 0, v[162:163]
	global_load_lds_dwordx4 v[190:191], off
	s_mov_b32 m0, s33
	v_lshl_add_u64 v[190:191], s[18:19], 0, v[164:165]
	global_load_lds_dwordx4 v[188:189], off
	v_lshl_add_u64 v[188:189], s[18:19], 0, v[168:169]
	s_mov_b32 m0, s28
	s_nop 0
	global_load_lds_dwordx4 v[188:189], off
	s_mov_b32 m0, s34
	s_nop 0
	global_load_lds_dwordx4 v[190:191], off
	s_waitcnt vmcnt(8)
	s_waitcnt lgkmcnt(0)
	s_barrier
	s_setprio 1
	s_waitcnt lgkmcnt(0)
	v_mfma_scale_f32_16x16x128_f8f6f4 v[82:85], v[24:31], v[226:233], 0, v220, v220 op_sel_hi:[0,0,0]
	v_mfma_scale_f32_16x16x128_f8f6f4 v[86:89], v[16:23], v[226:233], 0, v220, v220 op_sel_hi:[0,0,0]
	v_mfma_scale_f32_16x16x128_f8f6f4 v[66:69], v[24:31], v[234:241], 0, v220, v220 op_sel_hi:[0,0,0]
	v_mfma_scale_f32_16x16x128_f8f6f4 v[70:73], v[16:23], v[234:241], 0, v220, v220 op_sel_hi:[0,0,0]
	v_mfma_scale_f32_16x16x128_f8f6f4 v[50:53], v[24:31], v[242:249], 0, v220, v220 op_sel_hi:[0,0,0]
	v_mfma_scale_f32_16x16x128_f8f6f4 v[54:57], v[16:23], v[242:249], 0, v220, v220 op_sel_hi:[0,0,0]
	v_mfma_scale_f32_16x16x128_f8f6f4 v[24:27], v[24:31], v[212:219], 0, v220, v220 op_sel_hi:[0,0,0]
	v_mfma_scale_f32_16x16x128_f8f6f4 v[16:19], v[16:23], v[212:219], 0, v220, v220 op_sel_hi:[0,0,0]
	s_setprio 0
	s_setprio 1
	v_mfma_scale_f32_16x16x128_f8f6f4 v[20:23], v[0:7], v[226:233], 0, v220, v220 op_sel_hi:[0,0,0]
	v_mfma_scale_f32_16x16x128_f8f6f4 v[28:31], v[8:15], v[226:233], 0, v220, v220 op_sel_hi:[0,0,0]
	v_mfma_scale_f32_16x16x128_f8f6f4 v[74:77], v[0:7], v[234:241], 0, v220, v220 op_sel_hi:[0,0,0]
	v_mfma_scale_f32_16x16x128_f8f6f4 v[78:81], v[8:15], v[234:241], 0, v220, v220 op_sel_hi:[0,0,0]
	v_mfma_scale_f32_16x16x128_f8f6f4 v[58:61], v[0:7], v[242:249], 0, v220, v220 op_sel_hi:[0,0,0]
	v_mfma_scale_f32_16x16x128_f8f6f4 v[62:65], v[8:15], v[242:249], 0, v220, v220 op_sel_hi:[0,0,0]
	v_mfma_scale_f32_16x16x128_f8f6f4 v[42:45], v[0:7], v[212:219], 0, v220, v220 op_sel_hi:[0,0,0]
	v_mfma_scale_f32_16x16x128_f8f6f4 v[46:49], v[8:15], v[212:219], 0, v220, v220 op_sel_hi:[0,0,0]
	s_setprio 0
	s_barrier
; #define PG8_STAGE(bufoff, gbase, voff) do { _Pragma("unroll") for (int _i = 0; _i < 2; ++_i) \
;         __builtin_amdgcn_global_load_lds((const unsigned*)((const char*)(gbase) + (voff)[_i]), (LAS unsigned*)(lds + (bufoff) + ldsw + _i * 8192), 16, 0, 0); } while (0)
; #define PG8_STAGE_A(bufoff, h, abase) do { _Pragma("unroll") for (int _i = 0; _i < 2; ++_i) { \
;         const char* _src = GATHER ? ((const char*)(abase) + gA[h][_i]) : ((const char*)(abase) + (size_t)(h) * hstep + voffA[_i]); \
;         __builtin_amdgcn_global_load_lds((const unsigned*)_src, (LAS unsigned*)(lds + (bufoff) + ldsw + _i * 8192), 16, 0, 0); } } while (0)
; #define PG8_LDA(dst, b, h) do { _Pragma("unroll") for (int m = 0; m < 4; ++m) PG8_LD2(dst[m], PG8_SA(b, h) + aoff + m * 2048); } while (0)
; #define PG8_LDB(dst, b, h) do { _Pragma("unroll") for (int n = 0; n < 2; ++n) PG8_LD2(dst[n], PG8_SB(b, h) + boff + n * 2048); } while (0)
; #define PG8_WAIT_V(n) asm volatile("s_waitcnt vmcnt(" #n ")" ::: "memory")
; #define PG8_WAIT_L(n) asm volatile("s_waitcnt lgkmcnt(" #n ")" ::: "memory")
; #define PG8_BAR __builtin_amdgcn_s_barrier()
; #define PG8_SCHED __builtin_amdgcn_sched_barrier(0)
; template <int DT  , class Epi, class Sched, class Hook = NoHook>
; __device__ __forceinline__ void gemm_phase(LAS unsigned char* lds, const Sched& S, const Epi& E, int wave_s, LAS unsigned char* aux  ,
;                                            const Hook& H = Hook()  ) {
;     ...
;             PG8_WAIT_V(8); PG8_WAIT_L(0); PG8_BAR; PG8_MMA(1, 0, At, B0); PG8_MMA(1, 1, At, B1); PG8_BAR; PG8_SCHED;
;             PG8_LDB(B0, 1, 0); PG8_LDB(B1, 1, 1); PG8_SCHED; PG8_LDA(At, 1, 0); PG8_STAGE_A(PG8_SA(0, 1), 1, a2);
;             PG8_WAIT_V(8); PG8_WAIT_L(0); PG8_BAR; PG8_MMA(0, 0, At, B0); PG8_MMA(0, 1, At, B1); PG8_BAR; PG8_SCHED;
;             PG8_LDA(At, 1, 1); PG8_STAGE(PG8_SB(1, 0), b3, voffB); PG8_STAGE(PG8_SB(1, 1), b3 + hstep, voffB); PG8_STAGE_A(PG8_SA(1, 0), 0, a3);
;             PG8_WAIT_V(8); PG8_WAIT_L(0); PG8_BAR; PG8_MMA(1, 0, At, B0); PG8_MMA(1, 1, At, B1); PG8_BAR; PG8_SCHED;
;         }
	ds_read_b128 v[38:41], v204
	ds_read_b128 v[90:93], v205
	ds_read_b128 v[34:37], v193
	ds_read_b128 v[0:3], v196
	ds_read_b128 v[94:97], v206
	ds_read_b128 v[4:7], v207
	ds_read_b128 v[8:11], v208
	ds_read_b128 v[12:15], v209
	s_add_u32 s18, s18, 0x20000
	s_addc_u32 s19, s19, 0
	s_mov_b32 m0, s35
	v_lshl_add_u64 v[194:195], s[18:19], 0, v[168:169]
	ds_read_b128 v[212:215], v210 offset:32768
	ds_read_b128 v[216:219], v210 offset:33792
	ds_read_b128 v[226:229], v210 offset:34816
	ds_read_b128 v[230:233], v210 offset:35840
	ds_read_b128 v[234:237], v210 offset:36864
	ds_read_b128 v[238:241], v210 offset:37888
	ds_read_b128 v[242:245], v210 offset:38912
	ds_read_b128 v[246:249], v210 offset:39936
	global_load_lds_dwordx4 v[194:195], off
	v_lshl_add_u64 v[194:195], s[18:19], 0, v[164:165]
	s_mov_b32 m0, s38
	s_nop 0
	global_load_lds_dwordx4 v[194:195], off
	s_waitcnt vmcnt(8)
	s_waitcnt lgkmcnt(0)
	s_barrier
	s_setprio 1
	s_waitcnt lgkmcnt(0)
	v_mfma_scale_f32_16x16x128_f8f6f4 v[154:157], v[34:41], v[212:219], v[154:157], v220, v220 op_sel_hi:[0,0,0]
	v_mfma_scale_f32_16x16x128_f8f6f4 v[158:161], v[90:97], v[212:219], v[158:161], v220, v220 op_sel_hi:[0,0,0]
	v_mfma_scale_f32_16x16x128_f8f6f4 v[138:141], v[34:41], v[226:233], v[138:141], v220, v220 op_sel_hi:[0,0,0]
	v_mfma_scale_f32_16x16x128_f8f6f4 v[142:145], v[90:97], v[226:233], v[142:145], v220, v220 op_sel_hi:[0,0,0]
	v_mfma_scale_f32_16x16x128_f8f6f4 v[122:125], v[34:41], v[234:241], v[122:125], v220, v220 op_sel_hi:[0,0,0]
	v_mfma_scale_f32_16x16x128_f8f6f4 v[126:129], v[90:97], v[234:241], v[126:129], v220, v220 op_sel_hi:[0,0,0]
	v_mfma_scale_f32_16x16x128_f8f6f4 v[106:109], v[34:41], v[242:249], v[106:109], v220, v220 op_sel_hi:[0,0,0]
	v_mfma_scale_f32_16x16x128_f8f6f4 v[110:113], v[90:97], v[242:249], v[110:113], v220, v220 op_sel_hi:[0,0,0]
	s_setprio 0
	s_setprio 1
	v_mfma_scale_f32_16x16x128_f8f6f4 v[146:149], v[0:7], v[212:219], v[146:149], v220, v220 op_sel_hi:[0,0,0]
	v_mfma_scale_f32_16x16x128_f8f6f4 v[150:153], v[8:15], v[212:219], v[150:153], v220, v220 op_sel_hi:[0,0,0]
	v_mfma_scale_f32_16x16x128_f8f6f4 v[130:133], v[0:7], v[226:233], v[130:133], v220, v220 op_sel_hi:[0,0,0]
	v_mfma_scale_f32_16x16x128_f8f6f4 v[134:137], v[8:15], v[226:233], v[134:137], v220, v220 op_sel_hi:[0,0,0]
	v_mfma_scale_f32_16x16x128_f8f6f4 v[114:117], v[0:7], v[234:241], v[114:117], v220, v220 op_sel_hi:[0,0,0]
	v_mfma_scale_f32_16x16x128_f8f6f4 v[118:121], v[8:15], v[234:241], v[118:121], v220, v220 op_sel_hi:[0,0,0]
	v_mfma_scale_f32_16x16x128_f8f6f4 v[98:101], v[0:7], v[242:249], v[98:101], v220, v220 op_sel_hi:[0,0,0]
	v_mfma_scale_f32_16x16x128_f8f6f4 v[102:105], v[8:15], v[242:249], v[102:105], v220, v220 op_sel_hi:[0,0,0]
	s_setprio 0
	s_barrier
	s_mov_b32 m0, s40
	v_lshl_add_u64 v[184:185], v[184:185], 0, s[58:59]
	ds_read_b128 v[212:215], v210 offset:49152
	ds_read_b128 v[216:219], v210 offset:50176
	ds_read_b128 v[226:229], v210 offset:51200
	ds_read_b128 v[230:233], v210 offset:52224
	ds_read_b128 v[234:237], v210 offset:53248
	ds_read_b128 v[238:241], v210 offset:54272
	ds_read_b128 v[242:245], v210 offset:55296
	ds_read_b128 v[246:249], v210 offset:56320
	global_load_lds_dwordx4 v[184:185], off
	v_lshl_add_u64 v[184:185], v[186:187], 0, s[58:59]
	s_mov_b32 m0, s41
	v_lshl_add_u64 v[182:183], v[182:183], 0, s[62:63]
	global_load_lds_dwordx4 v[184:185], off
	v_lshl_add_u64 v[184:185], v[182:183], 0, v[166:167]
	s_mov_b32 m0, s46
	v_lshl_add_u64 v[182:183], v[182:183], 0, v[162:163]
	global_load_lds_dwordx4 v[184:185], off
	s_mov_b32 m0, s47
	s_nop 0
	global_load_lds_dwordx4 v[182:183], off
	v_lshl_add_u64 v[182:183], v[188:189], 0, s[58:59]
	s_mov_b32 m0, s44
	s_nop 0
	global_load_lds_dwordx4 v[182:183], off
	v_lshl_add_u64 v[182:183], v[190:191], 0, s[58:59]
	s_mov_b32 m0, s45
	s_nop 0
	global_load_lds_dwordx4 v[182:183], off
	s_waitcnt vmcnt(8)
	s_waitcnt lgkmcnt(0)
	s_barrier
	s_setprio 1
	s_waitcnt lgkmcnt(0)
	v_mfma_scale_f32_16x16x128_f8f6f4 v[82:85], v[34:41], v[212:219], v[82:85], v220, v220 op_sel_hi:[0,0,0]
	v_mfma_scale_f32_16x16x128_f8f6f4 v[86:89], v[90:97], v[212:219], v[86:89], v220, v220 op_sel_hi:[0,0,0]
	v_mfma_scale_f32_16x16x128_f8f6f4 v[66:69], v[34:41], v[226:233], v[66:69], v220, v220 op_sel_hi:[0,0,0]
	v_mfma_scale_f32_16x16x128_f8f6f4 v[70:73], v[90:97], v[226:233], v[70:73], v220, v220 op_sel_hi:[0,0,0]
	v_mfma_scale_f32_16x16x128_f8f6f4 v[50:53], v[34:41], v[234:241], v[50:53], v220, v220 op_sel_hi:[0,0,0]
	v_mfma_scale_f32_16x16x128_f8f6f4 v[54:57], v[90:97], v[234:241], v[54:57], v220, v220 op_sel_hi:[0,0,0]
	v_mfma_scale_f32_16x16x128_f8f6f4 v[34:37], v[34:41], v[242:249], v[24:27], v220, v220 op_sel_hi:[0,0,0]
	v_mfma_scale_f32_16x16x128_f8f6f4 v[38:41], v[90:97], v[242:249], v[16:19], v220, v220 op_sel_hi:[0,0,0]
	s_setprio 0
	s_setprio 1
	v_mfma_scale_f32_16x16x128_f8f6f4 v[90:93], v[0:7], v[212:219], v[20:23], v220, v220 op_sel_hi:[0,0,0]
	v_mfma_scale_f32_16x16x128_f8f6f4 v[94:97], v[8:15], v[212:219], v[28:31], v220, v220 op_sel_hi:[0,0,0]
	v_mfma_scale_f32_16x16x128_f8f6f4 v[74:77], v[0:7], v[226:233], v[74:77], v220, v220 op_sel_hi:[0,0,0]
	v_mfma_scale_f32_16x16x128_f8f6f4 v[78:81], v[8:15], v[226:233], v[78:81], v220, v220 op_sel_hi:[0,0,0]
	v_mfma_scale_f32_16x16x128_f8f6f4 v[58:61], v[0:7], v[234:241], v[58:61], v220, v220 op_sel_hi:[0,0,0]
	v_mfma_scale_f32_16x16x128_f8f6f4 v[62:65], v[8:15], v[234:241], v[62:65], v220, v220 op_sel_hi:[0,0,0]
	v_mfma_scale_f32_16x16x128_f8f6f4 v[42:45], v[0:7], v[242:249], v[42:45], v220, v220 op_sel_hi:[0,0,0]
	v_mfma_scale_f32_16x16x128_f8f6f4 v[46:49], v[8:15], v[242:249], v[46:49], v220, v220 op_sel_hi:[0,0,0]
	s_setprio 0
	s_barrier
	s_add_i32 s25, s25, 2
	s_add_u32 s22, s22, 0x100
	s_addc_u32 s23, s23, 0
	s_cmp_gt_u32 s25, 5
	v_lshl_add_u64 v[180:181], v[180:181], 0, s[54:55]
